# gate-epilogue row phases: loop-invariant gate bias loaded once before the block loop (lanes 0-7) instead of a load + vmcnt(0) wait in every row
# speedup vs baseline: 1.0000x; 1.0000x over previous
; template <int YMODE, int EXTRA, bool NORM_OUT, bool XN8  , bool XIN_BF = false  , bool XOUT_BF = false  > ...
;     ...
;     if (EXTRA) {
;         for (int k = F.tid; k < D; k += NTHR) { const f32x4 a = *(const f32x4*)(wex + (size_t)k * ldw), b = *(const f32x4*)(wex + (size_t)k * ldw + 4);
;             we[0 * D + k] = a[0]; we[1 * D + k] = a[1]; we[2 * D + k] = a[2]; we[3 * D + k] = a[3]; we[4 * D + k] = b[0]; we[5 * D + k] = b[1]; we[6 * D + k] = b[2]; we[7 * D + k] = b[3]; }
;     }
;     if (YMODE == 2) { if (F.tid == 0) { int cum = 0; for (int e = 0; e < NE; ++e) { cumt[e] = cum; cum += (int)((__hip_atomic_load(cntw + e, __ATOMIC_RELAXED, __HIP_MEMORY_SCOPE_AGENT) + 255u) >> 8); } } }
;     for (int blk = blockIdx.x; blk < M / 64; blk += F.G) {
;     ...
;                         if (F.lane < 8) { const float bb = (F.lane < 4) ? bi[F.lane] : bfg[F.lane - 4]; const float z = 15.f * tanhf((v + bb) * (1.f / 15.f));
;                             const float o = (F.lane < 4) ? z : (fminf(z, 0.f) - log1pf(expf(-fabsf(z)))); gates_out[row * 8 + F.lane] = o; }
.LBB0_101:
	v_lshl_add_u64 v[16:17], v[2:3], 0, s[12:13]
	v_lshl_add_u64 v[18:19], v[16:17], 0, s[12:13]
	v_lshl_add_u64 v[20:21], v[18:19], 0, s[12:13]
	global_load_dwordx4 v[22:25], v[2:3], off offset:-16
	global_load_dwordx4 v[26:29], v[2:3], off
	global_load_dwordx4 v[30:33], v[16:17], off offset:-16
	global_load_dwordx4 v[34:37], v[16:17], off
	global_load_dwordx4 v[38:41], v[18:19], off offset:-16
	global_load_dwordx4 v[42:45], v[18:19], off
	global_load_dwordx4 v[46:49], v[20:21], off offset:-16
	global_load_dwordx4 v[50:53], v[20:21], off
	s_waitcnt vmcnt(0)
	ds_write2st64_b32 v5, v22, v23 offset1:32
	ds_write2st64_b32 v5, v24, v25 offset0:64 offset1:96
	ds_write2st64_b32 v5, v26, v27 offset0:128 offset1:160
	ds_write2st64_b32 v5, v28, v29 offset0:192 offset1:224
	v_add_u32_e32 v5, 0x800, v5
	ds_write2st64_b32 v5, v30, v31 offset1:32
	ds_write2st64_b32 v5, v32, v33 offset0:64 offset1:96
	ds_write2st64_b32 v5, v34, v35 offset0:128 offset1:160
	ds_write2st64_b32 v5, v36, v37 offset0:192 offset1:224
	v_add_u32_e32 v5, 0x800, v5
	ds_write2st64_b32 v5, v38, v39 offset1:32
	ds_write2st64_b32 v5, v40, v41 offset0:64 offset1:96
	ds_write2st64_b32 v5, v42, v43 offset0:128 offset1:160
	ds_write2st64_b32 v5, v44, v45 offset0:192 offset1:224
	v_add_u32_e32 v5, 0x800, v5
	ds_write2st64_b32 v5, v46, v47 offset1:32
	ds_write2st64_b32 v5, v48, v49 offset0:64 offset1:96
	ds_write2st64_b32 v5, v50, v51 offset0:128 offset1:160
	ds_write2st64_b32 v5, v52, v53 offset0:192 offset1:224
	s_cmpk_gt_i32 s2, 0xff
	s_cbranch_scc1 .LBB0_120
	v_lshlrev_b32_e32 v66, 2, v1
	v_mov_b32_e32 v67, 0
	v_lshl_add_u64 v[68:69], s[8:9], 0, v[66:67]
	v_lshl_add_u64 v[2:3], s[50:51], 0, v[66:67]
	s_mov_b64 s[8:9], 0x102000
	s_add_u32 s3, s50, 0x400000
	v_lshl_add_u64 v[70:71], v[2:3], 0, s[8:9]
	s_mov_b64 s[8:9], 0x100000
	s_addc_u32 s4, s51, 0
	s_add_i32 s10, 0, 0x12000
	v_lshl_add_u64 v[72:73], v[2:3], 0, s[8:9]
	s_add_i32 s8, 0, 0x14000
	v_add_u32_e32 v84, s10, v66
	v_add_u32_e32 v85, s8, v66
	v_lshlrev_b32_e32 v66, 2, v194
	v_lshlrev_b32_e32 v2, 4, v194
	v_mov_b32_e32 v3, v67
	v_lshl_add_u64 v[4:5], s[28:29], 0, v[66:67]
	v_lshl_add_u64 v[74:75], s[6:7], 0, v[2:3]
	v_add_u32_e32 v86, s10, v2
	v_add_u32_e32 v87, s8, v2
	v_add_u32_e32 v88, 0, v2
	v_lshl_add_u64 v[2:3], s[26:27], 0, v[66:67]
	v_lshl_add_u64 v[4:5], v[4:5], 0, -16
	v_cmp_gt_u32_e32 vcc, 4, v194
	s_mov_b64 s[26:27], 0x200000
	v_readlane_b32 s5, v255, 9
	v_cndmask_b32_e32 v77, v5, v3, vcc
	v_cndmask_b32_e32 v76, v4, v2, vcc
	v_lshl_add_u64 v[2:3], s[50:51], 0, v[66:67]
	v_lshl_add_u64 v[78:79], v[2:3], 0, s[26:27]
	s_mov_b64 s[26:27], 0x18a00000
	s_lshl_b32 s5, s5, 3
	v_cmp_eq_u32_e64 s[6:7], 0, v194
	v_cmp_gt_u32_e64 s[8:9], 8, v194
	v_cmp_eq_u32_e64 s[10:11], 7, v194
	v_cmp_eq_u32_e64 s[12:13], 6, v194
	v_cmp_eq_u32_e64 s[14:15], 5, v194
	v_cmp_eq_u32_e64 s[16:17], 4, v194
	v_cmp_eq_u32_e64 s[18:19], 3, v194
	v_cmp_eq_u32_e64 s[20:21], 2, v194
	v_cmp_eq_u32_e64 s[22:23], 1, v194
	v_cmp_lt_u32_e64 s[24:25], 3, v194
	v_lshl_add_u64 v[80:81], v[2:3], 0, s[26:27]
	v_mov_b32_e32 v66, 0x358637bd
	s_mov_b32 s33, 0xf800000
	v_mov_b32_e32 v89, 0x260
	s_mov_b32 s40, 0x42fe0000
	s_mov_b32 s41, 0xc2fe0000
	s_mov_b32 s42, 0x40c0c00
	s_mov_b32 s43, 0x3f200000
	s_mov_b32 s44, 0x3fb8aa3b
	s_mov_b32 s45, 0xc2ce8ed0
	s_mov_b32 s46, 0x42b17218
	s_mov_b32 s47, 0x7f800000
	v_mov_b32_e32 v90, 0x3ca908c9
	s_brev_b32 s49, -2
	s_mov_b32 s52, 0xbfb8aa3b
	s_mov_b32 s53, 0xb2a5705f
	s_mov_b32 s54, 0x42ce8ed0
	s_mov_b32 s55, 0xc2b17218
	s_mov_b32 s56, 0x3f2aaaab
	v_mov_b32_e32 v91, 0x3ecc95a3
	s_mov_b32 s57, 0x3f317218
	s_mov_b32 s58, 0x33800000
	v_mov_b32_e32 v92, 0x3a000000
	v_mov_b32_e32 v93, 0x42fe0000
	v_mov_b32_e32 v94, 0x7f800000
	v_mov_b32_e32 v82, 0x3f317218
	s_mov_b32 s28, s2
	s_and_saveexec_b64 s[26:27], s[8:9]
	global_load_dword v153, v[76:77], off
	s_mov_b64 exec, s[26:27]
	s_branch .LBB0_105

; #define LAS __attribute__((address_space(3)))
; __device__ __forceinline__ unsigned cvtpk(float lo, float hi) { f32x2 v = {lo, hi}; bf16x2_t b = __builtin_convertvector(v, bf16x2_t); return __builtin_bit_cast(unsigned, b); }
; __device__ __forceinline__ float wave_max(float v) { return lane63(scan64<true>(v)); }
; template <int YMODE, int EXTRA, bool NORM_OUT, bool XN8  , bool XIN_BF = false  , bool XOUT_BF = false  > ...
;     ...
;                 if (XN8) {
;                     float am = 0.f;
; #pragma unroll
;                     for (int j = 0; j < 8; ++j) am = fmaxf(fmaxf(am, fmaxf(fabsf(x[j][0]), fabsf(x[j][1]))), fmaxf(fabsf(x[j][2]), fabsf(x[j][3])));
;                     am = wave_max(am);
;                     const float inv = am > 0.f ? 127.f / am : 0.f;
;                     if (F.lane == 0) { rowmax[row] = am; if (EXTRA == 2) route[384 + rl] = am; }
; #pragma unroll
;                     for (int j = 0; j < 8; ++j) *(unsigned*)((unsigned char*)XN + row * D + 256 * j + 4 * F.lane) = pack_i8x4(x[j][0] * inv, x[j][1] * inv, x[j][2] * inv, x[j][3] * inv);
;                 } else {
; #pragma unroll
;                     for (int j = 0; j < 8; ++j) { u32x2 w; w.x = cvtpk(x[j][0], x[j][1]); w.y = cvtpk(x[j][2], x[j][3]); *(u32x2*)(XN + row * D + 256 * j + 4 * F.lane) = w; }
;                 }
;                 if (EXTRA) {
;                     float d8[8];
; #pragma unroll
;                     for (int e = 0; e < 8; ++e) { float s = 0.f;
; #pragma unroll
;                         for (int j = 0; j < 8; ++j) { const f32x4 w = *(const LAS f32x4*)(we + e * D + 256 * j + 4 * F.lane); s += (x[j][0] * w[0] + x[j][1] * w[1]) + (x[j][2] * w[2] + x[j][3] * w[3]); }
.LBB0_112:
	s_or_b64 exec, exec, s[36:37]
	ds_read_b128 v[196:199], v88
	ds_read_b128 v[200:203], v88 offset:1024
	ds_read_b128 v[204:207], v88 offset:2048
	ds_read_b128 v[208:211], v88 offset:3072
	ds_read_b128 v[212:215], v88 offset:4096
	ds_read_b128 v[216:219], v88 offset:5120
	ds_read_b128 v[220:223], v88 offset:6144
	ds_read_b128 v[224:227], v88 offset:7168
	ds_read_b128 v[228:231], v88 offset:8192
	ds_read_b128 v[232:235], v88 offset:9216
	ds_read_b128 v[240:243], v88 offset:10240
	ds_read_b128 v[244:247], v88 offset:11264
	v_div_scale_f32 v1, s[36:37], s34, s34, v93
	v_rcp_f32_e32 v83, v1
	v_mov_b32_e32 v95, s34
	v_div_scale_f32 v95, vcc, s40, v95, s40
	v_fma_f32 v96, -v1, v83, 1.0
	v_fmac_f32_e32 v83, v96, v83
	v_mul_f32_e32 v96, v95, v83
	v_fma_f32 v97, -v1, v96, v95
	v_fmac_f32_e32 v96, v97, v83
	v_fma_f32 v1, -v1, v96, v95
	v_div_fmas_f32 v1, v1, v83, v96
	v_div_fixup_f32 v1, v1, s34, v93
	v_cmp_gt_f32_e64 vcc, s34, 0
	s_lshl_b64 s[36:37], s[26:27], 11
	v_lshl_add_u64 v[100:101], v[80:81], 0, s[36:37]
	v_cndmask_b32_e32 v1, 0, v1, vcc
	v_mul_f32_e32 v95, v65, v1
	v_mul_f32_e32 v83, v64, v1
	v_mul_f32_e32 v96, v62, v1
	v_mul_f32_e32 v97, v63, v1
	v_med3_f32 v95, v95, s41, v93
	v_med3_f32 v83, v83, s41, v93
	v_rndne_f32_e32 v95, v95
	v_med3_f32 v96, v96, s41, v93
	v_med3_f32 v97, v97, s41, v93
	v_rndne_f32_e32 v83, v83
	v_cvt_i32_f32_e32 v95, v95
	v_rndne_f32_e32 v96, v96
	v_rndne_f32_e32 v97, v97
	v_cvt_i32_f32_e32 v83, v83
	v_cvt_i32_f32_sdwa v96, v96 dst_sel:WORD_1 dst_unused:UNUSED_PAD src0_sel:DWORD
	v_cvt_i32_f32_e32 v97, v97
	v_lshlrev_b32_e32 v95, 8, v95
	v_and_b32_e32 v95, 0xff00, v95
	v_and_b32_e32 v96, 0xff0000, v96
	v_perm_b32 v83, v97, v83, s42
	v_or3_b32 v83, v83, v95, v96
	v_mul_f32_e32 v95, v61, v1
	global_store_dword v[100:101], v83, off
	v_mul_f32_e32 v83, v60, v1
	v_mul_f32_e32 v96, v58, v1
	v_mul_f32_e32 v97, v59, v1
	v_med3_f32 v95, v95, s41, v93
	v_med3_f32 v83, v83, s41, v93
	v_rndne_f32_e32 v95, v95
	v_med3_f32 v96, v96, s41, v93
	v_med3_f32 v97, v97, s41, v93
	v_rndne_f32_e32 v83, v83
	v_cvt_i32_f32_e32 v95, v95
	v_rndne_f32_e32 v96, v96
	v_rndne_f32_e32 v97, v97
	v_cvt_i32_f32_e32 v83, v83
	v_cvt_i32_f32_sdwa v96, v96 dst_sel:WORD_1 dst_unused:UNUSED_PAD src0_sel:DWORD
	v_cvt_i32_f32_e32 v97, v97
	v_lshlrev_b32_e32 v95, 8, v95
	v_and_b32_e32 v95, 0xff00, v95
	v_and_b32_e32 v96, 0xff0000, v96
	v_perm_b32 v83, v97, v83, s42
	v_or3_b32 v83, v83, v95, v96
	v_mul_f32_e32 v95, v57, v1
	global_store_dword v[100:101], v83, off offset:256
	v_mul_f32_e32 v83, v56, v1
	v_mul_f32_e32 v96, v54, v1
	v_mul_f32_e32 v97, v55, v1
	v_med3_f32 v95, v95, s41, v93
	v_med3_f32 v83, v83, s41, v93
	v_rndne_f32_e32 v95, v95
	v_med3_f32 v96, v96, s41, v93
	v_med3_f32 v97, v97, s41, v93
	v_rndne_f32_e32 v83, v83
	v_cvt_i32_f32_e32 v95, v95
	v_rndne_f32_e32 v96, v96
	v_rndne_f32_e32 v97, v97
	v_cvt_i32_f32_e32 v83, v83
	v_cvt_i32_f32_sdwa v96, v96 dst_sel:WORD_1 dst_unused:UNUSED_PAD src0_sel:DWORD
	v_cvt_i32_f32_e32 v97, v97
	v_lshlrev_b32_e32 v95, 8, v95
	v_and_b32_e32 v95, 0xff00, v95
	v_and_b32_e32 v96, 0xff0000, v96
	v_perm_b32 v83, v97, v83, s42
	v_or3_b32 v83, v83, v95, v96
	v_mul_f32_e32 v95, v53, v1
	global_store_dword v[100:101], v83, off offset:512
	v_mul_f32_e32 v83, v52, v1
	v_mul_f32_e32 v96, v50, v1
	v_mul_f32_e32 v97, v51, v1
	v_med3_f32 v95, v95, s41, v93
	v_med3_f32 v83, v83, s41, v93
	v_rndne_f32_e32 v95, v95
	v_med3_f32 v96, v96, s41, v93
	v_med3_f32 v97, v97, s41, v93
	v_rndne_f32_e32 v83, v83
	v_cvt_i32_f32_e32 v95, v95
	v_rndne_f32_e32 v96, v96
	v_rndne_f32_e32 v97, v97
	v_cvt_i32_f32_e32 v83, v83
	v_cvt_i32_f32_sdwa v96, v96 dst_sel:WORD_1 dst_unused:UNUSED_PAD src0_sel:DWORD
	v_cvt_i32_f32_e32 v97, v97
	v_lshlrev_b32_e32 v95, 8, v95
	v_and_b32_e32 v95, 0xff00, v95
	v_and_b32_e32 v96, 0xff0000, v96
	v_perm_b32 v83, v97, v83, s42
	v_or3_b32 v83, v83, v95, v96
	v_mul_f32_e32 v95, v49, v1
	global_store_dword v[100:101], v83, off offset:768
	v_mul_f32_e32 v83, v48, v1
	v_mul_f32_e32 v96, v46, v1
	v_mul_f32_e32 v97, v47, v1
	v_med3_f32 v95, v95, s41, v93
	v_med3_f32 v83, v83, s41, v93
	v_rndne_f32_e32 v95, v95
	v_med3_f32 v96, v96, s41, v93
	v_med3_f32 v97, v97, s41, v93
	v_rndne_f32_e32 v83, v83
	v_cvt_i32_f32_e32 v95, v95
	v_rndne_f32_e32 v96, v96
	v_rndne_f32_e32 v97, v97
	v_cvt_i32_f32_e32 v83, v83
	v_cvt_i32_f32_sdwa v96, v96 dst_sel:WORD_1 dst_unused:UNUSED_PAD src0_sel:DWORD
	v_cvt_i32_f32_e32 v97, v97
	v_lshlrev_b32_e32 v95, 8, v95
	v_and_b32_e32 v95, 0xff00, v95
	v_and_b32_e32 v96, 0xff0000, v96
	v_perm_b32 v83, v97, v83, s42
	v_or3_b32 v83, v83, v95, v96
	v_mul_f32_e32 v95, v45, v1
	global_store_dword v[100:101], v83, off offset:1024
	v_mul_f32_e32 v83, v44, v1
	v_mul_f32_e32 v96, v42, v1
	v_mul_f32_e32 v97, v43, v1
	v_med3_f32 v95, v95, s41, v93
	v_med3_f32 v83, v83, s41, v93
	v_rndne_f32_e32 v95, v95
	v_med3_f32 v96, v96, s41, v93
	v_med3_f32 v97, v97, s41, v93
	v_rndne_f32_e32 v83, v83
	v_cvt_i32_f32_e32 v95, v95
	v_rndne_f32_e32 v96, v96
	v_rndne_f32_e32 v97, v97
	v_cvt_i32_f32_e32 v83, v83
	v_cvt_i32_f32_sdwa v96, v96 dst_sel:WORD_1 dst_unused:UNUSED_PAD src0_sel:DWORD
	v_cvt_i32_f32_e32 v97, v97
	v_lshlrev_b32_e32 v95, 8, v95
	v_and_b32_e32 v95, 0xff00, v95
	v_and_b32_e32 v96, 0xff0000, v96
	v_perm_b32 v83, v97, v83, s42
	v_or3_b32 v83, v83, v95, v96
	v_mul_f32_e32 v95, v41, v1
	global_store_dword v[100:101], v83, off offset:1280
	v_mul_f32_e32 v83, v40, v1
	v_mul_f32_e32 v96, v38, v1
	v_mul_f32_e32 v97, v39, v1
	v_med3_f32 v95, v95, s41, v93
	v_med3_f32 v83, v83, s41, v93
	v_rndne_f32_e32 v95, v95
	v_med3_f32 v96, v96, s41, v93
	v_med3_f32 v97, v97, s41, v93
	v_rndne_f32_e32 v83, v83
	v_cvt_i32_f32_e32 v95, v95
	v_rndne_f32_e32 v96, v96
	v_rndne_f32_e32 v97, v97
	v_cvt_i32_f32_e32 v83, v83
	v_cvt_i32_f32_sdwa v96, v96 dst_sel:WORD_1 dst_unused:UNUSED_PAD src0_sel:DWORD
	v_cvt_i32_f32_e32 v97, v97
	v_lshlrev_b32_e32 v95, 8, v95
	v_and_b32_e32 v95, 0xff00, v95
	v_and_b32_e32 v96, 0xff0000, v96
	v_perm_b32 v83, v97, v83, s42
	v_or3_b32 v83, v83, v95, v96
	v_mul_f32_e32 v95, v37, v1
	v_mul_f32_e32 v96, v34, v1
	global_store_dword v[100:101], v83, off offset:1536
	v_mul_f32_e32 v83, v36, v1
	v_mul_f32_e32 v1, v35, v1
	v_med3_f32 v95, v95, s41, v93
	v_med3_f32 v96, v96, s41, v93
	v_med3_f32 v83, v83, s41, v93
	v_rndne_f32_e32 v95, v95
	v_rndne_f32_e32 v96, v96
	v_med3_f32 v1, v1, s41, v93
	v_rndne_f32_e32 v83, v83
	v_cvt_i32_f32_e32 v95, v95
	v_cvt_i32_f32_sdwa v96, v96 dst_sel:WORD_1 dst_unused:UNUSED_PAD src0_sel:DWORD
	v_rndne_f32_e32 v1, v1
	v_cvt_i32_f32_e32 v83, v83
	v_cvt_i32_f32_e32 v1, v1
	v_lshlrev_b32_e32 v95, 8, v95
	v_and_b32_e32 v102, 0xff0000, v96
	s_nop 0
	v_and_b32_e32 v95, 0xff00, v95
	v_perm_b32 v1, v1, v83, s42
	v_or3_b32 v1, v1, v95, v102
	global_store_dword v[100:101], v1, off offset:1792
	s_nop 0
	s_waitcnt lgkmcnt(12)
; #define LAS __attribute__((address_space(3)))
; __device__ __forceinline__ float wave_sum(float v) { return lane63(scan64<false>(v)); }
; template <int YMODE, int EXTRA, bool NORM_OUT, bool XN8  , bool XIN_BF = false  , bool XOUT_BF = false  > ...
;     ...
;                     float d8[8];
; #pragma unroll
;                     for (int e = 0; e < 8; ++e) { float s = 0.f;
; #pragma unroll
;                         for (int j = 0; j < 8; ++j) { const f32x4 w = *(const LAS f32x4*)(we + e * D + 256 * j + 4 * F.lane); s += (x[j][0] * w[0] + x[j][1] * w[1]) + (x[j][2] * w[2] + x[j][3] * w[3]); }
;                         d8[e] = wave_sum(s); asm volatile("" ::: "memory"); }
	s_waitcnt lgkmcnt(11)
	v_pk_mul_f32 v[190:191], v[64:65], v[196:197]
	ds_read_b128 v[248:251], v88 offset:12288
	v_pk_fma_f32 v[190:191], v[62:63], v[198:199], v[190:191]
	s_waitcnt lgkmcnt(11)
	v_pk_fma_f32 v[190:191], v[60:61], v[200:201], v[190:191]
	ds_read_b128 v[196:199], v88 offset:13312
	v_pk_fma_f32 v[190:191], v[58:59], v[202:203], v[190:191]
	s_waitcnt lgkmcnt(11)
	v_pk_fma_f32 v[190:191], v[56:57], v[204:205], v[190:191]
	ds_read_b128 v[200:203], v88 offset:14336
	v_pk_fma_f32 v[190:191], v[54:55], v[206:207], v[190:191]
	s_waitcnt lgkmcnt(11)
	v_pk_fma_f32 v[190:191], v[52:53], v[208:209], v[190:191]
	ds_read_b128 v[204:207], v88 offset:15360
	v_pk_fma_f32 v[190:191], v[50:51], v[210:211], v[190:191]
	s_waitcnt lgkmcnt(11)
	v_pk_fma_f32 v[190:191], v[48:49], v[212:213], v[190:191]
	ds_read_b128 v[208:211], v88 offset:16384
	v_pk_fma_f32 v[190:191], v[46:47], v[214:215], v[190:191]
	s_waitcnt lgkmcnt(11)
	v_pk_fma_f32 v[190:191], v[44:45], v[216:217], v[190:191]
	ds_read_b128 v[212:215], v88 offset:17408
	v_pk_fma_f32 v[190:191], v[42:43], v[218:219], v[190:191]
	s_waitcnt lgkmcnt(11)
	v_pk_fma_f32 v[190:191], v[40:41], v[220:221], v[190:191]
	ds_read_b128 v[216:219], v88 offset:18432
	v_pk_fma_f32 v[190:191], v[38:39], v[222:223], v[190:191]
	s_waitcnt lgkmcnt(11)
	v_pk_fma_f32 v[190:191], v[36:37], v[224:225], v[190:191]
	ds_read_b128 v[220:223], v88 offset:19456
	v_pk_fma_f32 v[190:191], v[34:35], v[226:227], v[190:191]
	v_add_f32_e32 v1, v190, v191
	v_mov_b32_e32 v83, 0
	s_nop 0
	s_nop 0
	v_add_f32_dpp v1, v1, v1 row_shr:1 row_mask:0xf bank_mask:0xf bound_ctrl:1
	s_nop 0
	s_waitcnt lgkmcnt(10)
	v_pk_mul_f32 v[192:193], v[60:61], v[232:233]
	ds_read_b128 v[224:227], v88 offset:20480
	v_pk_fma_f32 v[192:193], v[58:59], v[234:235], v[192:193]
	v_add_f32_dpp v1, v1, v1 row_shr:2 row_mask:0xf bank_mask:0xf bound_ctrl:1
	s_nop 0
	s_nop 0
	v_add_f32_dpp v1, v1, v1 row_shr:4 row_mask:0xf bank_mask:0xf bound_ctrl:1
	s_nop 1
	v_add_f32_dpp v1, v1, v1 row_shr:8 row_mask:0xf bank_mask:0xf bound_ctrl:1
	s_nop 1
	v_mov_b32_dpp v83, v1 row_bcast:15 row_mask:0xa bank_mask:0xf
	v_add_f32_e32 v1, v1, v83
	v_mov_b32_e32 v83, 0
	s_nop 1
	v_mov_b32_dpp v83, v1 row_bcast:31 row_mask:0xc bank_mask:0xf
	v_add_f32_e32 v1, v1, v83
	v_pk_fma_f32 v[192:193], v[64:65], v[228:229], v[192:193]
	ds_read_b128 v[232:235], v88 offset:21504
	v_pk_fma_f32 v[192:193], v[62:63], v[230:231], v[192:193]
	v_readlane_b32 s34, v1, 63
	s_nop 0
	s_nop 0
	s_nop 0
	s_waitcnt lgkmcnt(11)
	v_pk_fma_f32 v[192:193], v[56:57], v[240:241], v[192:193]
	ds_read_b128 v[228:231], v88 offset:22528
	v_pk_fma_f32 v[192:193], v[54:55], v[242:243], v[192:193]
	s_waitcnt lgkmcnt(11)
	v_pk_fma_f32 v[192:193], v[52:53], v[244:245], v[192:193]
	ds_read_b128 v[240:243], v88 offset:23552
	v_pk_fma_f32 v[192:193], v[50:51], v[246:247], v[192:193]
	s_waitcnt lgkmcnt(11)
	v_pk_fma_f32 v[192:193], v[48:49], v[248:249], v[192:193]
	ds_read_b128 v[244:247], v88 offset:24576
	v_pk_fma_f32 v[192:193], v[46:47], v[250:251], v[192:193]
	s_waitcnt lgkmcnt(11)
	v_pk_fma_f32 v[192:193], v[44:45], v[196:197], v[192:193]
	ds_read_b128 v[248:251], v88 offset:25600
	v_pk_fma_f32 v[192:193], v[42:43], v[198:199], v[192:193]
	s_waitcnt lgkmcnt(11)
	v_pk_fma_f32 v[192:193], v[40:41], v[200:201], v[192:193]
	ds_read_b128 v[196:199], v88 offset:26624
	v_pk_fma_f32 v[192:193], v[38:39], v[202:203], v[192:193]
	s_waitcnt lgkmcnt(11)
	v_pk_fma_f32 v[192:193], v[36:37], v[204:205], v[192:193]
	ds_read_b128 v[200:203], v88 offset:27648
	v_pk_fma_f32 v[192:193], v[34:35], v[206:207], v[192:193]
	v_add_f32_e32 v1, v192, v193
	v_mov_b32_e32 v83, 0
	s_nop 0
	s_nop 0
	v_add_f32_dpp v1, v1, v1 row_shr:1 row_mask:0xf bank_mask:0xf bound_ctrl:1
	s_nop 0
	s_waitcnt lgkmcnt(10)
	v_pk_mul_f32 v[190:191], v[60:61], v[212:213]
	ds_read_b128 v[204:207], v88 offset:28672
	v_pk_fma_f32 v[190:191], v[58:59], v[214:215], v[190:191]
	v_add_f32_dpp v1, v1, v1 row_shr:2 row_mask:0xf bank_mask:0xf bound_ctrl:1
	s_nop 0
	s_nop 0
	v_add_f32_dpp v1, v1, v1 row_shr:4 row_mask:0xf bank_mask:0xf bound_ctrl:1
	s_nop 1
	v_add_f32_dpp v1, v1, v1 row_shr:8 row_mask:0xf bank_mask:0xf bound_ctrl:1
	s_nop 1
	v_mov_b32_dpp v83, v1 row_bcast:15 row_mask:0xa bank_mask:0xf
	v_add_f32_e32 v1, v1, v83
	v_mov_b32_e32 v83, 0
	s_nop 1
	v_mov_b32_dpp v83, v1 row_bcast:31 row_mask:0xc bank_mask:0xf
	v_add_f32_e32 v1, v1, v83
	v_pk_fma_f32 v[190:191], v[64:65], v[208:209], v[190:191]
	ds_read_b128 v[212:215], v88 offset:29696
	v_pk_fma_f32 v[190:191], v[62:63], v[210:211], v[190:191]
	v_readlane_b32 s38, v1, 63
	s_nop 0
	s_nop 0
	s_nop 0
	s_waitcnt lgkmcnt(11)
	v_pk_fma_f32 v[190:191], v[56:57], v[216:217], v[190:191]
	ds_read_b128 v[208:211], v88 offset:30720
	v_pk_fma_f32 v[190:191], v[54:55], v[218:219], v[190:191]
	s_waitcnt lgkmcnt(11)
	v_pk_fma_f32 v[190:191], v[52:53], v[220:221], v[190:191]
	ds_read_b128 v[216:219], v88 offset:31744
	v_pk_fma_f32 v[190:191], v[50:51], v[222:223], v[190:191]
	s_waitcnt lgkmcnt(11)
	v_pk_fma_f32 v[190:191], v[48:49], v[224:225], v[190:191]
	ds_read_b128 v[220:223], v88 offset:32768
	v_pk_fma_f32 v[190:191], v[46:47], v[226:227], v[190:191]
	s_waitcnt lgkmcnt(11)
	v_pk_fma_f32 v[190:191], v[44:45], v[232:233], v[190:191]
	ds_read_b128 v[224:227], v88 offset:33792
	v_pk_fma_f32 v[190:191], v[42:43], v[234:235], v[190:191]
	s_waitcnt lgkmcnt(11)
	v_pk_fma_f32 v[190:191], v[40:41], v[228:229], v[190:191]
	ds_read_b128 v[232:235], v88 offset:34816
	v_pk_fma_f32 v[190:191], v[38:39], v[230:231], v[190:191]
	s_waitcnt lgkmcnt(11)
; #define LAS __attribute__((address_space(3)))
; __device__ __forceinline__ float wave_sum(float v) { return lane63(scan64<false>(v)); }
; template <int YMODE, int EXTRA, bool NORM_OUT, bool XN8  , bool XIN_BF = false  , bool XOUT_BF = false  > ...
;     ...
;                     float d8[8];
; #pragma unroll
;                     for (int e = 0; e < 8; ++e) { float s = 0.f;
; #pragma unroll
;                         for (int j = 0; j < 8; ++j) { const f32x4 w = *(const LAS f32x4*)(we + e * D + 256 * j + 4 * F.lane); s += (x[j][0] * w[0] + x[j][1] * w[1]) + (x[j][2] * w[2] + x[j][3] * w[3]); }
;                         d8[e] = wave_sum(s); asm volatile("" ::: "memory"); }
	v_pk_fma_f32 v[190:191], v[36:37], v[240:241], v[190:191]
	ds_read_b128 v[228:231], v88 offset:35840
	v_pk_fma_f32 v[190:191], v[34:35], v[242:243], v[190:191]
	v_add_f32_e32 v1, v190, v191
	v_mov_b32_e32 v83, 0
	s_nop 0
	s_nop 0
	v_add_f32_dpp v1, v1, v1 row_shr:1 row_mask:0xf bank_mask:0xf bound_ctrl:1
	s_nop 0
	s_waitcnt lgkmcnt(10)
	v_pk_mul_f32 v[192:193], v[60:61], v[248:249]
	ds_read_b128 v[240:243], v88 offset:36864
	v_pk_fma_f32 v[192:193], v[58:59], v[250:251], v[192:193]
	v_add_f32_dpp v1, v1, v1 row_shr:2 row_mask:0xf bank_mask:0xf bound_ctrl:1
	s_nop 0
	s_nop 0
	v_add_f32_dpp v1, v1, v1 row_shr:4 row_mask:0xf bank_mask:0xf bound_ctrl:1
	s_nop 1
	v_add_f32_dpp v1, v1, v1 row_shr:8 row_mask:0xf bank_mask:0xf bound_ctrl:1
	s_nop 1
	v_mov_b32_dpp v83, v1 row_bcast:15 row_mask:0xa bank_mask:0xf
	v_add_f32_e32 v1, v1, v83
	v_mov_b32_e32 v83, 0
	s_nop 1
	v_mov_b32_dpp v83, v1 row_bcast:31 row_mask:0xc bank_mask:0xf
	v_add_f32_e32 v1, v1, v83
	v_pk_fma_f32 v[192:193], v[64:65], v[244:245], v[192:193]
	ds_read_b128 v[248:251], v88 offset:37888
	v_pk_fma_f32 v[192:193], v[62:63], v[246:247], v[192:193]
	v_readlane_b32 s39, v1, 63
	s_nop 0
	s_nop 0
	s_nop 0
	s_waitcnt lgkmcnt(11)
	v_pk_fma_f32 v[192:193], v[56:57], v[196:197], v[192:193]
	ds_read_b128 v[244:247], v88 offset:38912
	v_pk_fma_f32 v[192:193], v[54:55], v[198:199], v[192:193]
	s_waitcnt lgkmcnt(11)
	v_pk_fma_f32 v[192:193], v[52:53], v[200:201], v[192:193]
	ds_read_b128 v[196:199], v88 offset:39936
	v_pk_fma_f32 v[192:193], v[50:51], v[202:203], v[192:193]
	s_waitcnt lgkmcnt(11)
	v_pk_fma_f32 v[192:193], v[48:49], v[204:205], v[192:193]
	ds_read_b128 v[200:203], v88 offset:40960
	v_pk_fma_f32 v[192:193], v[46:47], v[206:207], v[192:193]
	s_waitcnt lgkmcnt(11)
	v_pk_fma_f32 v[192:193], v[44:45], v[212:213], v[192:193]
	ds_read_b128 v[204:207], v88 offset:41984
	v_pk_fma_f32 v[192:193], v[42:43], v[214:215], v[192:193]
	s_waitcnt lgkmcnt(11)
	v_pk_fma_f32 v[192:193], v[40:41], v[208:209], v[192:193]
	ds_read_b128 v[212:215], v88 offset:43008
	v_pk_fma_f32 v[192:193], v[38:39], v[210:211], v[192:193]
	s_waitcnt lgkmcnt(11)
	v_pk_fma_f32 v[192:193], v[36:37], v[216:217], v[192:193]
	ds_read_b128 v[208:211], v88 offset:44032
	v_pk_fma_f32 v[192:193], v[34:35], v[218:219], v[192:193]
	v_add_f32_e32 v1, v192, v193
	v_mov_b32_e32 v83, 0
	s_nop 0
	s_nop 0
	v_add_f32_dpp v1, v1, v1 row_shr:1 row_mask:0xf bank_mask:0xf bound_ctrl:1
	s_nop 0
	s_waitcnt lgkmcnt(10)
	v_pk_mul_f32 v[190:191], v[60:61], v[224:225]
	ds_read_b128 v[216:219], v88 offset:45056
	v_pk_fma_f32 v[190:191], v[58:59], v[226:227], v[190:191]
	v_add_f32_dpp v1, v1, v1 row_shr:2 row_mask:0xf bank_mask:0xf bound_ctrl:1
	s_nop 0
	s_nop 0
	v_add_f32_dpp v1, v1, v1 row_shr:4 row_mask:0xf bank_mask:0xf bound_ctrl:1
	s_nop 1
	v_add_f32_dpp v1, v1, v1 row_shr:8 row_mask:0xf bank_mask:0xf bound_ctrl:1
	s_nop 1
	v_mov_b32_dpp v83, v1 row_bcast:15 row_mask:0xa bank_mask:0xf
	v_add_f32_e32 v1, v1, v83
	v_mov_b32_e32 v83, 0
	s_nop 1
	v_mov_b32_dpp v83, v1 row_bcast:31 row_mask:0xc bank_mask:0xf
	v_add_f32_e32 v1, v1, v83
	v_pk_fma_f32 v[190:191], v[64:65], v[220:221], v[190:191]
	ds_read_b128 v[224:227], v88 offset:46080
	v_pk_fma_f32 v[190:191], v[62:63], v[222:223], v[190:191]
	v_readlane_b32 s60, v1, 63
	s_nop 0
	s_nop 0
	s_nop 0
	s_waitcnt lgkmcnt(11)
	v_pk_fma_f32 v[190:191], v[56:57], v[232:233], v[190:191]
	ds_read_b128 v[220:223], v88 offset:47104
	v_pk_fma_f32 v[190:191], v[54:55], v[234:235], v[190:191]
	s_waitcnt lgkmcnt(11)
	v_pk_fma_f32 v[190:191], v[52:53], v[228:229], v[190:191]
	ds_read_b128 v[232:235], v88 offset:48128
	v_pk_fma_f32 v[190:191], v[50:51], v[230:231], v[190:191]
	s_waitcnt lgkmcnt(11)
	v_pk_fma_f32 v[190:191], v[48:49], v[240:241], v[190:191]
	ds_read_b128 v[228:231], v88 offset:49152
	v_pk_fma_f32 v[190:191], v[46:47], v[242:243], v[190:191]
	s_waitcnt lgkmcnt(11)
	v_pk_fma_f32 v[190:191], v[44:45], v[248:249], v[190:191]
	ds_read_b128 v[240:243], v88 offset:50176
	v_pk_fma_f32 v[190:191], v[42:43], v[250:251], v[190:191]
	s_waitcnt lgkmcnt(11)
	v_pk_fma_f32 v[190:191], v[40:41], v[244:245], v[190:191]
	ds_read_b128 v[248:251], v88 offset:51200
	v_pk_fma_f32 v[190:191], v[38:39], v[246:247], v[190:191]
	s_waitcnt lgkmcnt(11)
	v_pk_fma_f32 v[190:191], v[36:37], v[196:197], v[190:191]
	ds_read_b128 v[244:247], v88 offset:52224
	v_pk_fma_f32 v[190:191], v[34:35], v[198:199], v[190:191]
	v_add_f32_e32 v1, v190, v191
	v_mov_b32_e32 v83, 0
	s_nop 0
	s_nop 0
	v_add_f32_dpp v1, v1, v1 row_shr:1 row_mask:0xf bank_mask:0xf bound_ctrl:1
	s_nop 0
	s_waitcnt lgkmcnt(10)
	v_pk_mul_f32 v[192:193], v[60:61], v[204:205]
	ds_read_b128 v[196:199], v88 offset:53248
	v_pk_fma_f32 v[192:193], v[58:59], v[206:207], v[192:193]
	v_add_f32_dpp v1, v1, v1 row_shr:2 row_mask:0xf bank_mask:0xf bound_ctrl:1
	s_nop 0
	s_nop 0
	v_add_f32_dpp v1, v1, v1 row_shr:4 row_mask:0xf bank_mask:0xf bound_ctrl:1
	s_nop 1
	v_add_f32_dpp v1, v1, v1 row_shr:8 row_mask:0xf bank_mask:0xf bound_ctrl:1
	s_nop 1
	v_mov_b32_dpp v83, v1 row_bcast:15 row_mask:0xa bank_mask:0xf
	v_add_f32_e32 v1, v1, v83
	v_mov_b32_e32 v83, 0
	s_nop 1
	v_mov_b32_dpp v83, v1 row_bcast:31 row_mask:0xc bank_mask:0xf
	v_add_f32_e32 v1, v1, v83
	v_pk_fma_f32 v[192:193], v[64:65], v[200:201], v[192:193]
	ds_read_b128 v[204:207], v88 offset:54272
	v_pk_fma_f32 v[192:193], v[62:63], v[202:203], v[192:193]
	v_readlane_b32 s61, v1, 63
	s_nop 0
	s_nop 0
	s_nop 0
	s_waitcnt lgkmcnt(11)
	v_pk_fma_f32 v[192:193], v[56:57], v[212:213], v[192:193]
	ds_read_b128 v[200:203], v88 offset:55296
	v_pk_fma_f32 v[192:193], v[54:55], v[214:215], v[192:193]
	s_waitcnt lgkmcnt(11)
; #define LAS __attribute__((address_space(3)))
; __device__ __forceinline__ float wave_sum(float v) { return lane63(scan64<false>(v)); }
; template <int YMODE, int EXTRA, bool NORM_OUT, bool XN8  , bool XIN_BF = false  , bool XOUT_BF = false  > ...
;     ...
;                     float d8[8];
; #pragma unroll
;                     for (int e = 0; e < 8; ++e) { float s = 0.f;
; #pragma unroll
;                         for (int j = 0; j < 8; ++j) { const f32x4 w = *(const LAS f32x4*)(we + e * D + 256 * j + 4 * F.lane); s += (x[j][0] * w[0] + x[j][1] * w[1]) + (x[j][2] * w[2] + x[j][3] * w[3]); }
;                         d8[e] = wave_sum(s); asm volatile("" ::: "memory"); }
;                     if (EXTRA == 1) {
;                         float v = 0.f;
; #pragma unroll
;                         for (int e = 0; e < 8; ++e) v = (F.lane == e) ? d8[e] : v;
;                         if (F.lane < 8) { const float bb = (F.lane < 4) ? bi[F.lane] : bfg[F.lane - 4]; const float z = 15.f * tanhf((v + bb) * (1.f / 15.f));
;                             const float o = (F.lane < 4) ? z : (fminf(z, 0.f) - log1pf(expf(-fabsf(z)))); gates_out[row * 8 + F.lane] = o; }
	v_pk_fma_f32 v[192:193], v[52:53], v[208:209], v[192:193]
	ds_read_b128 v[212:215], v88 offset:56320
	v_pk_fma_f32 v[192:193], v[50:51], v[210:211], v[192:193]
	s_waitcnt lgkmcnt(11)
	v_pk_fma_f32 v[192:193], v[48:49], v[216:217], v[192:193]
	ds_read_b128 v[208:211], v88 offset:57344
	v_pk_fma_f32 v[192:193], v[46:47], v[218:219], v[192:193]
	s_waitcnt lgkmcnt(11)
	v_pk_fma_f32 v[192:193], v[44:45], v[224:225], v[192:193]
	ds_read_b128 v[216:219], v88 offset:58368
	v_pk_fma_f32 v[192:193], v[42:43], v[226:227], v[192:193]
	s_waitcnt lgkmcnt(11)
	v_pk_fma_f32 v[192:193], v[40:41], v[220:221], v[192:193]
	ds_read_b128 v[224:227], v88 offset:59392
	v_pk_fma_f32 v[192:193], v[38:39], v[222:223], v[192:193]
	s_waitcnt lgkmcnt(11)
	v_pk_fma_f32 v[192:193], v[36:37], v[232:233], v[192:193]
	ds_read_b128 v[220:223], v88 offset:60416
	v_pk_fma_f32 v[192:193], v[34:35], v[234:235], v[192:193]
	v_add_f32_e32 v1, v192, v193
	v_mov_b32_e32 v83, 0
	s_nop 0
	s_nop 0
	v_add_f32_dpp v1, v1, v1 row_shr:1 row_mask:0xf bank_mask:0xf bound_ctrl:1
	s_nop 0
	s_waitcnt lgkmcnt(10)
	v_pk_mul_f32 v[190:191], v[60:61], v[240:241]
	ds_read_b128 v[232:235], v88 offset:61440
	v_pk_fma_f32 v[190:191], v[58:59], v[242:243], v[190:191]
	v_add_f32_dpp v1, v1, v1 row_shr:2 row_mask:0xf bank_mask:0xf bound_ctrl:1
	s_nop 0
	s_nop 0
	v_add_f32_dpp v1, v1, v1 row_shr:4 row_mask:0xf bank_mask:0xf bound_ctrl:1
	s_nop 1
	v_add_f32_dpp v1, v1, v1 row_shr:8 row_mask:0xf bank_mask:0xf bound_ctrl:1
	s_nop 1
	v_mov_b32_dpp v83, v1 row_bcast:15 row_mask:0xa bank_mask:0xf
	v_add_f32_e32 v1, v1, v83
	v_mov_b32_e32 v83, 0
	s_nop 1
	v_mov_b32_dpp v83, v1 row_bcast:31 row_mask:0xc bank_mask:0xf
	v_add_f32_e32 v1, v1, v83
	v_pk_fma_f32 v[190:191], v[64:65], v[228:229], v[190:191]
	ds_read_b128 v[240:243], v88 offset:62464
	v_pk_fma_f32 v[190:191], v[62:63], v[230:231], v[190:191]
	v_readlane_b32 s62, v1, 63
	s_nop 0
	s_nop 0
	s_nop 0
	s_waitcnt lgkmcnt(11)
	v_pk_fma_f32 v[190:191], v[56:57], v[248:249], v[190:191]
	ds_read_b128 v[228:231], v88 offset:63488
	v_pk_fma_f32 v[190:191], v[54:55], v[250:251], v[190:191]
	s_waitcnt lgkmcnt(11)
	v_pk_fma_f32 v[190:191], v[52:53], v[244:245], v[190:191]
	ds_read_b128 v[248:251], v88 offset:64512
	v_pk_fma_f32 v[190:191], v[50:51], v[246:247], v[190:191]
	s_waitcnt lgkmcnt(11)
	v_pk_fma_f32 v[190:191], v[48:49], v[196:197], v[190:191]
	v_pk_fma_f32 v[190:191], v[46:47], v[198:199], v[190:191]
	s_waitcnt lgkmcnt(10)
	v_pk_fma_f32 v[190:191], v[44:45], v[204:205], v[190:191]
	v_pk_fma_f32 v[190:191], v[42:43], v[206:207], v[190:191]
	s_waitcnt lgkmcnt(9)
	v_pk_fma_f32 v[190:191], v[40:41], v[200:201], v[190:191]
	v_pk_fma_f32 v[190:191], v[38:39], v[202:203], v[190:191]
	s_waitcnt lgkmcnt(8)
	v_pk_fma_f32 v[190:191], v[36:37], v[212:213], v[190:191]
	v_pk_fma_f32 v[190:191], v[34:35], v[214:215], v[190:191]
	v_add_f32_e32 v1, v190, v191
	v_mov_b32_e32 v83, 0
	s_nop 0
	s_nop 0
	v_add_f32_dpp v1, v1, v1 row_shr:1 row_mask:0xf bank_mask:0xf bound_ctrl:1
	s_nop 0
	s_waitcnt lgkmcnt(7)
	v_pk_mul_f32 v[192:193], v[64:65], v[208:209]
	v_pk_fma_f32 v[192:193], v[62:63], v[210:211], v[192:193]
	v_add_f32_dpp v1, v1, v1 row_shr:2 row_mask:0xf bank_mask:0xf bound_ctrl:1
	s_waitcnt lgkmcnt(6)
	v_pk_fma_f32 v[192:193], v[60:61], v[216:217], v[192:193]
	v_pk_fma_f32 v[192:193], v[58:59], v[218:219], v[192:193]
	v_add_f32_dpp v1, v1, v1 row_shr:4 row_mask:0xf bank_mask:0xf bound_ctrl:1
	s_nop 0
	s_nop 0
	v_add_f32_dpp v1, v1, v1 row_shr:8 row_mask:0xf bank_mask:0xf bound_ctrl:1
	s_nop 1
	v_mov_b32_dpp v83, v1 row_bcast:15 row_mask:0xa bank_mask:0xf
	v_add_f32_e32 v1, v1, v83
	v_mov_b32_e32 v83, 0
	s_nop 1
	v_mov_b32_dpp v83, v1 row_bcast:31 row_mask:0xc bank_mask:0xf
	v_add_f32_e32 v1, v1, v83
	s_nop 0
	v_readlane_b32 s63, v1, 63
	s_nop 0
	s_nop 0
	s_nop 0
	s_waitcnt lgkmcnt(5)
	v_pk_fma_f32 v[192:193], v[56:57], v[224:225], v[192:193]
	v_pk_fma_f32 v[192:193], v[54:55], v[226:227], v[192:193]
	s_waitcnt lgkmcnt(4)
	v_pk_fma_f32 v[192:193], v[52:53], v[220:221], v[192:193]
	v_pk_fma_f32 v[192:193], v[50:51], v[222:223], v[192:193]
	s_waitcnt lgkmcnt(3)
	v_pk_fma_f32 v[192:193], v[48:49], v[232:233], v[192:193]
	v_pk_fma_f32 v[192:193], v[46:47], v[234:235], v[192:193]
	s_waitcnt lgkmcnt(2)
	v_pk_fma_f32 v[192:193], v[44:45], v[240:241], v[192:193]
	v_pk_fma_f32 v[192:193], v[42:43], v[242:243], v[192:193]
	s_waitcnt lgkmcnt(1)
	v_pk_fma_f32 v[192:193], v[40:41], v[228:229], v[192:193]
	v_pk_fma_f32 v[192:193], v[38:39], v[230:231], v[192:193]
	s_waitcnt lgkmcnt(0)
	v_pk_fma_f32 v[192:193], v[36:37], v[248:249], v[192:193]
	v_pk_fma_f32 v[192:193], v[34:35], v[250:251], v[192:193]
	v_add_f32_e32 v1, v192, v193
	v_mov_b32_e32 v34, 0
	s_nop 0
	v_add_f32_dpp v1, v1, v1 row_shr:1 row_mask:0xf bank_mask:0xf bound_ctrl:1
	s_nop 1
	v_add_f32_dpp v1, v1, v1 row_shr:2 row_mask:0xf bank_mask:0xf bound_ctrl:1
	s_nop 1
	v_add_f32_dpp v1, v1, v1 row_shr:4 row_mask:0xf bank_mask:0xf bound_ctrl:1
	s_nop 1
	v_add_f32_dpp v1, v1, v1 row_shr:8 row_mask:0xf bank_mask:0xf bound_ctrl:1
	s_nop 1
	v_mov_b32_dpp v34, v1 row_bcast:15 row_mask:0xa bank_mask:0xf
	v_add_f32_e32 v1, v1, v34
	v_mov_b32_e32 v34, 0
	s_nop 1
	v_mov_b32_dpp v34, v1 row_bcast:31 row_mask:0xc bank_mask:0xf
	v_add_f32_e32 v1, v1, v34
	s_nop 0
	v_readlane_b32 s64, v1, 63
	s_and_saveexec_b64 s[36:37], s[8:9]
	s_cbranch_execz .LBB0_107
	v_mov_b32_e32 v34, s34
	v_cndmask_b32_e64 v34, 0, v34, s[6:7]
	v_mov_b32_e32 v35, s38
	v_cndmask_b32_e64 v34, v34, v35, s[22:23]
	v_mov_b32_e32 v35, s39
	v_cndmask_b32_e64 v34, v34, v35, s[20:21]
	v_mov_b32_e32 v35, s60
	v_cndmask_b32_e64 v34, v34, v35, s[18:19]
	v_mov_b32_e32 v35, s61
	v_cndmask_b32_e64 v34, v34, v35, s[16:17]
	v_mov_b32_e32 v35, s62
	v_cndmask_b32_e64 v34, v34, v35, s[14:15]
	v_mov_b32_e32 v35, s63
	v_cndmask_b32_e64 v34, v34, v35, s[12:13]
	v_mov_b32_e32 v35, s64
	v_cndmask_b32_e64 v34, v34, v35, s[10:11]
	s_waitcnt lgkmcnt(0)
	v_add_f32_e32 v1, v34, v153
	v_mul_f32_e32 v1, 0x3d888889, v1
	v_cmp_nlt_f32_e64 s[38:39], |v1|, s43
	s_and_saveexec_b64 s[60:61], s[38:39]
	s_xor_b64 s[38:39], exec, s[60:61]
	s_cbranch_execz .LBB0_115
	v_add_f32_e64 v34, |v1|, |v1|
	v_mul_f32_e32 v35, 0x3fb8aa3b, v34
	v_rndne_f32_e32 v36, v35
	v_sub_f32_e32 v37, v35, v36
	v_fma_f32 v35, v34, s44, -v35
	v_fmac_f32_e32 v35, 0x32a5705f, v34
	v_add_f32_e32 v35, v37, v35
	v_cvt_i32_f32_e32 v36, v36
	v_exp_f32_e32 v35, v35
	v_cmp_ngt_f32_e32 vcc, s45, v34
	v_ldexp_f32 v35, v35, v36
	s_nop 0
	v_cndmask_b32_e32 v35, 0, v35, vcc
	v_cmp_nlt_f32_e32 vcc, s46, v34
	s_nop 1
	v_cndmask_b32_e32 v34, v94, v35, vcc
	v_add_f32_e32 v34, 1.0, v34
	v_rcp_f32_e32 v34, v34
	s_nop 0
	v_fma_f32 v34, v34, -2.0, 1.0

; template <int YMODE, int EXTRA, bool NORM_OUT, bool XN8  , bool XIN_BF = false  , bool XOUT_BF = false  > ...
;     ...
;     if (EXTRA) {
;         for (int k = F.tid; k < D; k += NTHR) { const f32x4 a = *(const f32x4*)(wex + (size_t)k * ldw), b = *(const f32x4*)(wex + (size_t)k * ldw + 4);
;             we[0 * D + k] = a[0]; we[1 * D + k] = a[1]; we[2 * D + k] = a[2]; we[3 * D + k] = a[3]; we[4 * D + k] = b[0]; we[5 * D + k] = b[1]; we[6 * D + k] = b[2]; we[7 * D + k] = b[3]; }
;     }
;     if (YMODE == 2) { if (F.tid == 0) { int cum = 0; for (int e = 0; e < NE; ++e) { cumt[e] = cum; cum += (int)((__hip_atomic_load(cntw + e, __ATOMIC_RELAXED, __HIP_MEMORY_SCOPE_AGENT) + 255u) >> 8); } } }
;     for (int blk = blockIdx.x; blk < M / 64; blk += F.G) {
;     ...
;                         if (F.lane < 8) { const float bb = (F.lane < 4) ? bi[F.lane] : bfg[F.lane - 4]; const float z = 15.f * tanhf((v + bb) * (1.f / 15.f));
;                             const float o = (F.lane < 4) ? z : (fminf(z, 0.f) - log1pf(expf(-fabsf(z)))); gates_out[row * 8 + F.lane] = o; }
.LBB0_1300:
	v_lshl_add_u64 v[16:17], v[2:3], 0, s[10:11]
	v_lshl_add_u64 v[18:19], v[16:17], 0, s[10:11]
	v_lshl_add_u64 v[20:21], v[18:19], 0, s[10:11]
	global_load_dwordx4 v[22:25], v[2:3], off offset:-16
	global_load_dwordx4 v[26:29], v[2:3], off
	global_load_dwordx4 v[30:33], v[16:17], off offset:-16
	global_load_dwordx4 v[34:37], v[16:17], off
	global_load_dwordx4 v[38:41], v[18:19], off offset:-16
	global_load_dwordx4 v[42:45], v[18:19], off
	global_load_dwordx4 v[46:49], v[20:21], off offset:-16
	global_load_dwordx4 v[50:53], v[20:21], off
	s_waitcnt vmcnt(0)
	ds_write2st64_b32 v5, v22, v23 offset1:32
	ds_write2st64_b32 v5, v24, v25 offset0:64 offset1:96
	ds_write2st64_b32 v5, v26, v27 offset0:128 offset1:160
	ds_write2st64_b32 v5, v28, v29 offset0:192 offset1:224
	v_add_u32_e32 v5, 0x800, v5
	ds_write2st64_b32 v5, v30, v31 offset1:32
	ds_write2st64_b32 v5, v32, v33 offset0:64 offset1:96
	ds_write2st64_b32 v5, v34, v35 offset0:128 offset1:160
	ds_write2st64_b32 v5, v36, v37 offset0:192 offset1:224
	v_add_u32_e32 v5, 0x800, v5
	ds_write2st64_b32 v5, v38, v39 offset1:32
	ds_write2st64_b32 v5, v40, v41 offset0:64 offset1:96
	ds_write2st64_b32 v5, v42, v43 offset0:128 offset1:160
	ds_write2st64_b32 v5, v44, v45 offset0:192 offset1:224
	v_add_u32_e32 v5, 0x800, v5
	ds_write2st64_b32 v5, v46, v47 offset1:32
	ds_write2st64_b32 v5, v48, v49 offset0:64 offset1:96
	ds_write2st64_b32 v5, v50, v51 offset0:128 offset1:160
	ds_write2st64_b32 v5, v52, v53 offset0:192 offset1:224
	s_cmpk_gt_i32 s2, 0xff
	s_cbranch_scc1 .LBB0_1318
	s_add_u32 s3, s50, 0x400000
	v_lshlrev_b32_e32 v2, 2, v1
	v_mov_b32_e32 v3, 0
	s_addc_u32 s4, s51, 0
	v_lshl_add_u64 v[8:9], s[0:1], 0, v[2:3]
	s_mov_b64 s[0:1], 0x2000
	s_add_u32 s30, s12, 16
	v_lshl_add_u64 v[12:13], s[50:51], 0, v[2:3]
	v_lshl_add_u64 v[8:9], v[8:9], 0, s[0:1]
	s_mov_b64 s[0:1], 0x162000
	s_addc_u32 s31, s13, 0
	s_mov_b64 s[8:9], 0x10a000
	v_lshl_add_u64 v[6:7], s[6:7], 0, v[2:3]
	s_add_i32 s6, 0, 0x10000
	v_lshl_add_u64 v[10:11], v[12:13], 0, s[0:1]
	s_mov_b64 s[0:1], 0x160000
	v_lshl_add_u64 v[4:5], v[12:13], 0, s[8:9]
	v_add_u32_e32 v100, s6, v2
	s_add_i32 s6, 0, 0x12000
	v_lshl_add_u64 v[12:13], v[12:13], 0, s[0:1]
	s_add_i32 s7, 0, 0x14000
	v_readlane_b32 s0, v255, 9
	v_lshlrev_b32_e32 v16, 3, v194
	v_mov_b32_e32 v17, v3
	v_lshlrev_b32_e32 v1, 4, v194
	s_lshl_b32 s40, s0, 3
	v_lshl_add_u64 v[14:15], s[50:51], 0, v[16:17]
	s_mov_b64 s[0:1], 0x32a00000
	v_add_u32_e32 v103, s6, v1
	v_add_u32_e32 v104, s7, v1
	v_add_u32_e32 v105, 0, v1
	v_mov_b32_e32 v1, s27
	v_mov_b32_e32 v18, s31
	v_cmp_gt_u32_e32 vcc, 4, v194
	v_lshl_add_u64 v[14:15], v[14:15], 0, s[0:1]
	v_readlane_b32 s0, v255, 15
	v_cndmask_b32_e32 v19, v1, v18, vcc
	v_mov_b32_e32 v1, s26
	v_mov_b32_e32 v18, s30
	v_add_u32_e32 v101, s6, v2
	v_add_u32_e32 v102, s7, v2
	v_lshlrev_b32_e32 v2, 2, v194
	v_cndmask_b32_e32 v18, v1, v18, vcc
	v_readlane_b32 s1, v255, 16
	v_lshl_add_u64 v[16:17], s[72:73], 0, v[16:17]
	v_cmp_eq_u32_e64 s[6:7], 0, v194
	v_cmp_gt_u32_e64 s[8:9], 8, v194
	v_cmp_eq_u32_e64 s[10:11], 7, v194
	v_cmp_eq_u32_e64 s[12:13], 6, v194
	v_cmp_eq_u32_e64 s[14:15], 5, v194
	v_cmp_eq_u32_e64 s[16:17], 4, v194
	v_cmp_eq_u32_e64 s[18:19], 3, v194
	v_cmp_eq_u32_e64 s[20:21], 2, v194
	v_cmp_eq_u32_e64 s[22:23], 1, v194
	v_cmp_lt_u32_e64 s[24:25], 3, v194
	v_lshl_add_u64 v[18:19], v[18:19], 0, v[2:3]
	v_lshl_add_u64 v[20:21], s[0:1], 0, v[2:3]
	v_lshl_add_u64 v[22:23], s[60:61], 0, v[2:3]
	v_mov_b32_e32 v2, 0x358637bd
	s_mov_b32 s41, 0xf800000
	v_mov_b32_e32 v106, 0x260
	s_mov_b32 s42, 0xc2fe0000
	s_mov_b32 s43, 0x40c0c00
	s_mov_b32 s44, 0x42b17218
	s_mov_b32 s45, 0x7f800000
	v_mov_b32_e32 v107, 0x3ca908c9
	s_brev_b32 s46, -2
	s_mov_b32 s47, 0xbfb8aa3b
	s_mov_b32 s49, 0xb2a5705f
	s_mov_b32 s52, 0x42ce8ed0
	s_mov_b32 s53, 0xc2b17218
	s_mov_b32 s54, 0x3f2aaaab
	v_mov_b32_e32 v108, 0x3ecc95a3
	s_mov_b32 s55, 0x3f317218
	s_mov_b32 s56, 0x33800000
	v_mov_b32_e32 v109, 0x3a000000
	v_mov_b32_e32 v110, 0x42fe0000
	v_mov_b32_e32 v111, 0x7f800000
	v_mov_b32_e32 v24, 0x3f317218
	s_mov_b32 s0, s2
	s_and_saveexec_b64 s[26:27], s[8:9]
	global_load_dword v179, v[18:19], off
	s_mov_b64 exec, s[26:27]
	s_branch .LBB0_1304

; #define LAS __attribute__((address_space(3)))
; __device__ __forceinline__ unsigned cvtpk(float lo, float hi) { f32x2 v = {lo, hi}; bf16x2_t b = __builtin_convertvector(v, bf16x2_t); return __builtin_bit_cast(unsigned, b); }
; __device__ __forceinline__ float wave_max(float v) { return lane63(scan64<true>(v)); }
; template <int YMODE, int EXTRA, bool NORM_OUT, bool XN8  , bool XIN_BF = false  , bool XOUT_BF = false  > ...
;     ...
;                 if (XN8) {
;                     float am = 0.f;
; #pragma unroll
;                     for (int j = 0; j < 8; ++j) am = fmaxf(fmaxf(am, fmaxf(fabsf(x[j][0]), fabsf(x[j][1]))), fmaxf(fabsf(x[j][2]), fabsf(x[j][3])));
;                     am = wave_max(am);
;                     const float inv = am > 0.f ? 127.f / am : 0.f;
;                     if (F.lane == 0) { rowmax[row] = am; if (EXTRA == 2) route[384 + rl] = am; }
; #pragma unroll
;                     for (int j = 0; j < 8; ++j) *(unsigned*)((unsigned char*)XN + row * D + 256 * j + 4 * F.lane) = pack_i8x4(x[j][0] * inv, x[j][1] * inv, x[j][2] * inv, x[j][3] * inv);
;                 } else {
; #pragma unroll
;                     for (int j = 0; j < 8; ++j) { u32x2 w; w.x = cvtpk(x[j][0], x[j][1]); w.y = cvtpk(x[j][2], x[j][3]); *(u32x2*)(XN + row * D + 256 * j + 4 * F.lane) = w; }
;                 }
;                 if (EXTRA) {
;                     float d8[8];
; #pragma unroll
;                     for (int e = 0; e < 8; ++e) { float s = 0.f;
; #pragma unroll
;                         for (int j = 0; j < 8; ++j) { const f32x4 w = *(const LAS f32x4*)(we + e * D + 256 * j + 4 * F.lane); s += (x[j][0] * w[0] + x[j][1] * w[1]) + (x[j][2] * w[2] + x[j][3] * w[3]); }
.LBB0_1311:
	s_or_b64 exec, exec, s[26:27]
	ds_read_b128 v[196:199], v105
	ds_read_b128 v[200:203], v105 offset:1024
	ds_read_b128 v[204:207], v105 offset:2048
	ds_read_b128 v[208:211], v105 offset:3072
	ds_read_b128 v[212:215], v105 offset:4096
	ds_read_b128 v[216:219], v105 offset:5120
	ds_read_b128 v[220:223], v105 offset:6144
	ds_read_b128 v[224:227], v105 offset:7168
	ds_read_b128 v[228:231], v105 offset:8192
	ds_read_b128 v[232:235], v105 offset:9216
	ds_read_b128 v[240:243], v105 offset:10240
	ds_read_b128 v[244:247], v105 offset:11264
	v_div_scale_f32 v1, s[26:27], s34, s34, v110
	v_rcp_f32_e32 v25, v1
	v_mov_b32_e32 v90, s34
	s_mov_b32 s26, 0x42fe0000
	v_div_scale_f32 v90, vcc, s26, v90, s26
	v_fma_f32 v91, -v1, v25, 1.0
	v_fmac_f32_e32 v25, v91, v25
	v_mul_f32_e32 v91, v90, v25
	v_fma_f32 v92, -v1, v91, v90
	v_fmac_f32_e32 v91, v92, v25
	v_fma_f32 v1, -v1, v91, v90
	v_div_fmas_f32 v1, v1, v25, v91
	v_div_fixup_f32 v1, v1, s34, v110
	v_cmp_gt_f32_e64 vcc, s34, 0
	s_lshl_b64 s[26:27], s[36:37], 11
	v_lshl_add_u64 v[94:95], v[22:23], 0, s[26:27]
	v_cndmask_b32_e32 v1, 0, v1, vcc
	v_mul_f32_e32 v90, v85, v1
	v_mul_f32_e32 v25, v84, v1
	v_mul_f32_e32 v91, v72, v1
	v_mul_f32_e32 v92, v73, v1
	v_med3_f32 v90, v90, s42, v110
	v_med3_f32 v25, v25, s42, v110
	v_rndne_f32_e32 v90, v90
	v_med3_f32 v91, v91, s42, v110
	v_med3_f32 v92, v92, s42, v110
	v_rndne_f32_e32 v25, v25
	v_cvt_i32_f32_e32 v90, v90
	v_rndne_f32_e32 v91, v91
	v_rndne_f32_e32 v92, v92
	v_cvt_i32_f32_e32 v25, v25
	v_cvt_i32_f32_sdwa v91, v91 dst_sel:WORD_1 dst_unused:UNUSED_PAD src0_sel:DWORD
	v_cvt_i32_f32_e32 v92, v92
	v_lshlrev_b32_e32 v90, 8, v90
	v_and_b32_e32 v90, 0xff00, v90
	v_and_b32_e32 v91, 0xff0000, v91
	v_perm_b32 v25, v92, v25, s43
	v_or3_b32 v25, v25, v90, v91
	v_mul_f32_e32 v90, v89, v1
	global_store_dword v[94:95], v25, off
	v_mul_f32_e32 v25, v88, v1
	v_mul_f32_e32 v91, v62, v1
	v_mul_f32_e32 v92, v63, v1
	v_med3_f32 v90, v90, s42, v110
	v_med3_f32 v25, v25, s42, v110
	v_rndne_f32_e32 v90, v90
	v_med3_f32 v91, v91, s42, v110
	v_med3_f32 v92, v92, s42, v110
	v_rndne_f32_e32 v25, v25
	v_cvt_i32_f32_e32 v90, v90
	v_rndne_f32_e32 v91, v91
	v_rndne_f32_e32 v92, v92
	v_cvt_i32_f32_e32 v25, v25
	v_cvt_i32_f32_sdwa v91, v91 dst_sel:WORD_1 dst_unused:UNUSED_PAD src0_sel:DWORD
	v_cvt_i32_f32_e32 v92, v92
	v_lshlrev_b32_e32 v90, 8, v90
	v_and_b32_e32 v90, 0xff00, v90
	v_and_b32_e32 v91, 0xff0000, v91
	v_perm_b32 v25, v92, v25, s43
	v_or3_b32 v25, v25, v90, v91
	v_mul_f32_e32 v90, v81, v1
	global_store_dword v[94:95], v25, off offset:256
	v_mul_f32_e32 v25, v80, v1
	v_mul_f32_e32 v91, v70, v1
	v_mul_f32_e32 v92, v71, v1
	v_med3_f32 v90, v90, s42, v110
	v_med3_f32 v25, v25, s42, v110
	v_rndne_f32_e32 v90, v90
	v_med3_f32 v91, v91, s42, v110
	v_med3_f32 v92, v92, s42, v110
	v_rndne_f32_e32 v25, v25
	v_cvt_i32_f32_e32 v90, v90
	v_rndne_f32_e32 v91, v91
	v_rndne_f32_e32 v92, v92
	v_cvt_i32_f32_e32 v25, v25
	v_cvt_i32_f32_sdwa v91, v91 dst_sel:WORD_1 dst_unused:UNUSED_PAD src0_sel:DWORD
	v_cvt_i32_f32_e32 v92, v92
	v_lshlrev_b32_e32 v90, 8, v90
	v_and_b32_e32 v90, 0xff00, v90
	v_and_b32_e32 v91, 0xff0000, v91
	v_perm_b32 v25, v92, v25, s43
	v_or3_b32 v25, v25, v90, v91
	v_mul_f32_e32 v90, v87, v1
	global_store_dword v[94:95], v25, off offset:512
	v_mul_f32_e32 v25, v86, v1
	v_mul_f32_e32 v91, v60, v1
	v_mul_f32_e32 v92, v61, v1
	v_med3_f32 v90, v90, s42, v110
	v_med3_f32 v25, v25, s42, v110
	v_rndne_f32_e32 v90, v90
	v_med3_f32 v91, v91, s42, v110
	v_med3_f32 v92, v92, s42, v110
	v_rndne_f32_e32 v25, v25
	v_cvt_i32_f32_e32 v90, v90
	v_rndne_f32_e32 v91, v91
	v_rndne_f32_e32 v92, v92
	v_cvt_i32_f32_e32 v25, v25
	v_cvt_i32_f32_sdwa v91, v91 dst_sel:WORD_1 dst_unused:UNUSED_PAD src0_sel:DWORD
	v_cvt_i32_f32_e32 v92, v92
	v_lshlrev_b32_e32 v90, 8, v90
	v_and_b32_e32 v90, 0xff00, v90
	v_and_b32_e32 v91, 0xff0000, v91
	v_perm_b32 v25, v92, v25, s43
	v_or3_b32 v25, v25, v90, v91
	v_mul_f32_e32 v90, v77, v1
	global_store_dword v[94:95], v25, off offset:768
	v_mul_f32_e32 v25, v76, v1
	v_mul_f32_e32 v91, v68, v1
	v_mul_f32_e32 v92, v69, v1
	v_med3_f32 v90, v90, s42, v110
	v_med3_f32 v25, v25, s42, v110
	v_rndne_f32_e32 v90, v90
	v_med3_f32 v91, v91, s42, v110
	v_med3_f32 v92, v92, s42, v110
	v_rndne_f32_e32 v25, v25
	v_cvt_i32_f32_e32 v90, v90
	v_rndne_f32_e32 v91, v91
	v_rndne_f32_e32 v92, v92
	v_cvt_i32_f32_e32 v25, v25
	v_cvt_i32_f32_sdwa v91, v91 dst_sel:WORD_1 dst_unused:UNUSED_PAD src0_sel:DWORD
	v_cvt_i32_f32_e32 v92, v92
	v_lshlrev_b32_e32 v90, 8, v90
	v_and_b32_e32 v90, 0xff00, v90
	v_and_b32_e32 v91, 0xff0000, v91
	v_perm_b32 v25, v92, v25, s43
	v_or3_b32 v25, v25, v90, v91
	v_mul_f32_e32 v90, v83, v1
	global_store_dword v[94:95], v25, off offset:1024
	v_mul_f32_e32 v25, v82, v1
	v_mul_f32_e32 v91, v58, v1
	v_mul_f32_e32 v92, v59, v1
	v_med3_f32 v90, v90, s42, v110
	v_med3_f32 v25, v25, s42, v110
	v_rndne_f32_e32 v90, v90
	v_med3_f32 v91, v91, s42, v110
	v_med3_f32 v92, v92, s42, v110
	v_rndne_f32_e32 v25, v25
	v_cvt_i32_f32_e32 v90, v90
	v_rndne_f32_e32 v91, v91
	v_rndne_f32_e32 v92, v92
	v_cvt_i32_f32_e32 v25, v25
	v_cvt_i32_f32_sdwa v91, v91 dst_sel:WORD_1 dst_unused:UNUSED_PAD src0_sel:DWORD
	v_cvt_i32_f32_e32 v92, v92
	v_lshlrev_b32_e32 v90, 8, v90
	v_and_b32_e32 v90, 0xff00, v90
	v_and_b32_e32 v91, 0xff0000, v91
	v_perm_b32 v25, v92, v25, s43
	v_or3_b32 v25, v25, v90, v91
	v_mul_f32_e32 v90, v75, v1
	global_store_dword v[94:95], v25, off offset:1280
	v_mul_f32_e32 v25, v74, v1
	v_mul_f32_e32 v91, v64, v1
	v_mul_f32_e32 v92, v65, v1
	v_med3_f32 v90, v90, s42, v110
	v_med3_f32 v25, v25, s42, v110
	v_rndne_f32_e32 v90, v90
	v_med3_f32 v91, v91, s42, v110
	v_med3_f32 v92, v92, s42, v110
	v_rndne_f32_e32 v25, v25
	v_cvt_i32_f32_e32 v90, v90
	v_rndne_f32_e32 v91, v91
	v_rndne_f32_e32 v92, v92
	v_cvt_i32_f32_e32 v25, v25
	v_cvt_i32_f32_sdwa v91, v91 dst_sel:WORD_1 dst_unused:UNUSED_PAD src0_sel:DWORD
	v_cvt_i32_f32_e32 v92, v92
	v_lshlrev_b32_e32 v90, 8, v90
	v_and_b32_e32 v90, 0xff00, v90
	v_and_b32_e32 v91, 0xff0000, v91
	v_perm_b32 v25, v92, v25, s43
	v_or3_b32 v25, v25, v90, v91
	v_mul_f32_e32 v90, v79, v1
	global_store_dword v[94:95], v25, off offset:1536
	v_mul_f32_e32 v25, v78, v1
	v_mul_f32_e32 v91, v66, v1
	v_mul_f32_e32 v1, v67, v1
	v_med3_f32 v90, v90, s42, v110
	v_med3_f32 v25, v25, s42, v110
	v_rndne_f32_e32 v90, v90
	v_med3_f32 v91, v91, s42, v110
	v_med3_f32 v1, v1, s42, v110
	v_rndne_f32_e32 v25, v25
	v_cvt_i32_f32_e32 v90, v90
	v_rndne_f32_e32 v91, v91
	v_rndne_f32_e32 v1, v1
	v_cvt_i32_f32_e32 v25, v25
	v_cvt_i32_f32_sdwa v91, v91 dst_sel:WORD_1 dst_unused:UNUSED_PAD src0_sel:DWORD
	v_cvt_i32_f32_e32 v1, v1
	v_lshlrev_b32_e32 v90, 8, v90
	v_and_b32_e32 v96, 0xff00, v90
	v_and_b32_e32 v97, 0xff0000, v91
	s_nop 0
	v_perm_b32 v1, v1, v25, s43
	v_or3_b32 v1, v1, v96, v97
	global_store_dword v[94:95], v1, off offset:1792
	s_nop 0
	s_waitcnt lgkmcnt(12)
; #define LAS __attribute__((address_space(3)))
; __device__ __forceinline__ float wave_sum(float v) { return lane63(scan64<false>(v)); }
; template <int YMODE, int EXTRA, bool NORM_OUT, bool XN8  , bool XIN_BF = false  , bool XOUT_BF = false  > ...
;     ...
;                     float d8[8];
; #pragma unroll
;                     for (int e = 0; e < 8; ++e) { float s = 0.f;
; #pragma unroll
;                         for (int j = 0; j < 8; ++j) { const f32x4 w = *(const LAS f32x4*)(we + e * D + 256 * j + 4 * F.lane); s += (x[j][0] * w[0] + x[j][1] * w[1]) + (x[j][2] * w[2] + x[j][3] * w[3]); }
;                         d8[e] = wave_sum(s); asm volatile("" ::: "memory"); }
	s_waitcnt lgkmcnt(11)
	v_pk_mul_f32 v[190:191], v[84:85], v[196:197]
	ds_read_b128 v[248:251], v105 offset:12288
	v_pk_fma_f32 v[190:191], v[72:73], v[198:199], v[190:191]
	s_waitcnt lgkmcnt(11)
	v_pk_fma_f32 v[190:191], v[88:89], v[200:201], v[190:191]
	ds_read_b128 v[196:199], v105 offset:13312
	v_pk_fma_f32 v[190:191], v[62:63], v[202:203], v[190:191]
	s_waitcnt lgkmcnt(11)
	v_pk_fma_f32 v[190:191], v[80:81], v[204:205], v[190:191]
	ds_read_b128 v[200:203], v105 offset:14336
	v_pk_fma_f32 v[190:191], v[70:71], v[206:207], v[190:191]
	s_waitcnt lgkmcnt(11)
	v_pk_fma_f32 v[190:191], v[86:87], v[208:209], v[190:191]
	ds_read_b128 v[204:207], v105 offset:15360
	v_pk_fma_f32 v[190:191], v[60:61], v[210:211], v[190:191]
	s_waitcnt lgkmcnt(11)
	v_pk_fma_f32 v[190:191], v[76:77], v[212:213], v[190:191]
	ds_read_b128 v[208:211], v105 offset:16384
	v_pk_fma_f32 v[190:191], v[68:69], v[214:215], v[190:191]
	s_waitcnt lgkmcnt(11)
	v_pk_fma_f32 v[190:191], v[82:83], v[216:217], v[190:191]
	ds_read_b128 v[212:215], v105 offset:17408
	v_pk_fma_f32 v[190:191], v[58:59], v[218:219], v[190:191]
	s_waitcnt lgkmcnt(11)
	v_pk_fma_f32 v[190:191], v[74:75], v[220:221], v[190:191]
	ds_read_b128 v[216:219], v105 offset:18432
	v_pk_fma_f32 v[190:191], v[64:65], v[222:223], v[190:191]
	s_waitcnt lgkmcnt(11)
	v_pk_fma_f32 v[190:191], v[78:79], v[224:225], v[190:191]
	ds_read_b128 v[220:223], v105 offset:19456
	v_pk_fma_f32 v[190:191], v[66:67], v[226:227], v[190:191]
	v_add_f32_e32 v1, v190, v191
	v_mov_b32_e32 v25, 0
	s_nop 0
	s_nop 0
	v_add_f32_dpp v1, v1, v1 row_shr:1 row_mask:0xf bank_mask:0xf bound_ctrl:1
	s_nop 1
	v_add_f32_dpp v1, v1, v1 row_shr:2 row_mask:0xf bank_mask:0xf bound_ctrl:1
	s_nop 1
	v_add_f32_dpp v1, v1, v1 row_shr:4 row_mask:0xf bank_mask:0xf bound_ctrl:1
	s_nop 1
	v_add_f32_dpp v1, v1, v1 row_shr:8 row_mask:0xf bank_mask:0xf bound_ctrl:1
	s_nop 1
	v_mov_b32_dpp v25, v1 row_bcast:15 row_mask:0xa bank_mask:0xf
	v_add_f32_e32 v1, v1, v25
	v_mov_b32_e32 v25, 0
	s_nop 1
	v_mov_b32_dpp v25, v1 row_bcast:31 row_mask:0xc bank_mask:0xf
	v_add_f32_e32 v1, v1, v25
	s_nop 0
	s_waitcnt lgkmcnt(11)
	v_pk_mul_f32 v[192:193], v[84:85], v[228:229]
	ds_read_b128 v[224:227], v105 offset:20480
	v_pk_fma_f32 v[192:193], v[72:73], v[230:231], v[192:193]
	v_readlane_b32 s34, v1, 63
	s_nop 0
	s_nop 0
	s_waitcnt lgkmcnt(11)
	v_pk_fma_f32 v[192:193], v[88:89], v[232:233], v[192:193]
	ds_read_b128 v[228:231], v105 offset:21504
	v_pk_fma_f32 v[192:193], v[62:63], v[234:235], v[192:193]
	s_waitcnt lgkmcnt(11)
	v_pk_fma_f32 v[192:193], v[80:81], v[240:241], v[192:193]
	ds_read_b128 v[232:235], v105 offset:22528
	v_pk_fma_f32 v[192:193], v[70:71], v[242:243], v[192:193]
	s_waitcnt lgkmcnt(11)
	v_pk_fma_f32 v[192:193], v[86:87], v[244:245], v[192:193]
	ds_read_b128 v[240:243], v105 offset:23552
	v_pk_fma_f32 v[192:193], v[60:61], v[246:247], v[192:193]
	s_waitcnt lgkmcnt(11)
	v_pk_fma_f32 v[192:193], v[76:77], v[248:249], v[192:193]
	ds_read_b128 v[244:247], v105 offset:24576
	v_pk_fma_f32 v[192:193], v[68:69], v[250:251], v[192:193]
	s_waitcnt lgkmcnt(11)
	v_pk_fma_f32 v[192:193], v[82:83], v[196:197], v[192:193]
	ds_read_b128 v[248:251], v105 offset:25600
	v_pk_fma_f32 v[192:193], v[58:59], v[198:199], v[192:193]
	s_waitcnt lgkmcnt(11)
	v_pk_fma_f32 v[192:193], v[74:75], v[200:201], v[192:193]
	ds_read_b128 v[196:199], v105 offset:26624
	v_pk_fma_f32 v[192:193], v[64:65], v[202:203], v[192:193]
	s_waitcnt lgkmcnt(11)
	v_pk_fma_f32 v[192:193], v[78:79], v[204:205], v[192:193]
	ds_read_b128 v[200:203], v105 offset:27648
	v_pk_fma_f32 v[192:193], v[66:67], v[206:207], v[192:193]
	v_add_f32_e32 v1, v192, v193
	v_mov_b32_e32 v25, 0
	s_nop 0
	s_nop 0
	v_add_f32_dpp v1, v1, v1 row_shr:1 row_mask:0xf bank_mask:0xf bound_ctrl:1
	s_nop 1
	v_add_f32_dpp v1, v1, v1 row_shr:2 row_mask:0xf bank_mask:0xf bound_ctrl:1
	s_nop 1
	v_add_f32_dpp v1, v1, v1 row_shr:4 row_mask:0xf bank_mask:0xf bound_ctrl:1
	s_nop 1
	v_add_f32_dpp v1, v1, v1 row_shr:8 row_mask:0xf bank_mask:0xf bound_ctrl:1
	s_nop 1
	v_mov_b32_dpp v25, v1 row_bcast:15 row_mask:0xa bank_mask:0xf
	v_add_f32_e32 v1, v1, v25
	v_mov_b32_e32 v25, 0
	s_nop 1
	v_mov_b32_dpp v25, v1 row_bcast:31 row_mask:0xc bank_mask:0xf
	v_add_f32_e32 v1, v1, v25
	s_nop 0
	s_waitcnt lgkmcnt(11)
	v_pk_mul_f32 v[190:191], v[84:85], v[208:209]
	ds_read_b128 v[204:207], v105 offset:28672
	v_pk_fma_f32 v[190:191], v[72:73], v[210:211], v[190:191]
	v_readlane_b32 s38, v1, 63
	s_nop 0
	s_nop 0
	s_waitcnt lgkmcnt(11)
	v_pk_fma_f32 v[190:191], v[88:89], v[212:213], v[190:191]
	ds_read_b128 v[208:211], v105 offset:29696
	v_pk_fma_f32 v[190:191], v[62:63], v[214:215], v[190:191]
	s_waitcnt lgkmcnt(11)
	v_pk_fma_f32 v[190:191], v[80:81], v[216:217], v[190:191]
	ds_read_b128 v[212:215], v105 offset:30720
	v_pk_fma_f32 v[190:191], v[70:71], v[218:219], v[190:191]
	s_waitcnt lgkmcnt(11)
	v_pk_fma_f32 v[190:191], v[86:87], v[220:221], v[190:191]
	ds_read_b128 v[216:219], v105 offset:31744
	v_pk_fma_f32 v[190:191], v[60:61], v[222:223], v[190:191]
	s_waitcnt lgkmcnt(11)
	v_pk_fma_f32 v[190:191], v[76:77], v[224:225], v[190:191]
	ds_read_b128 v[220:223], v105 offset:32768
	v_pk_fma_f32 v[190:191], v[68:69], v[226:227], v[190:191]
	s_waitcnt lgkmcnt(11)
	v_pk_fma_f32 v[190:191], v[82:83], v[228:229], v[190:191]
	ds_read_b128 v[224:227], v105 offset:33792
	v_pk_fma_f32 v[190:191], v[58:59], v[230:231], v[190:191]
	s_waitcnt lgkmcnt(11)
	v_pk_fma_f32 v[190:191], v[74:75], v[232:233], v[190:191]
	ds_read_b128 v[228:231], v105 offset:34816
	v_pk_fma_f32 v[190:191], v[64:65], v[234:235], v[190:191]
	s_waitcnt lgkmcnt(11)
; #define LAS __attribute__((address_space(3)))
; __device__ __forceinline__ float wave_sum(float v) { return lane63(scan64<false>(v)); }
; template <int YMODE, int EXTRA, bool NORM_OUT, bool XN8  , bool XIN_BF = false  , bool XOUT_BF = false  > ...
;     ...
;                     float d8[8];
; #pragma unroll
;                     for (int e = 0; e < 8; ++e) { float s = 0.f;
; #pragma unroll
;                         for (int j = 0; j < 8; ++j) { const f32x4 w = *(const LAS f32x4*)(we + e * D + 256 * j + 4 * F.lane); s += (x[j][0] * w[0] + x[j][1] * w[1]) + (x[j][2] * w[2] + x[j][3] * w[3]); }
;                         d8[e] = wave_sum(s); asm volatile("" ::: "memory"); }
	v_pk_fma_f32 v[190:191], v[78:79], v[240:241], v[190:191]
	ds_read_b128 v[232:235], v105 offset:35840
	v_pk_fma_f32 v[190:191], v[66:67], v[242:243], v[190:191]
	v_add_f32_e32 v1, v190, v191
	v_mov_b32_e32 v25, 0
	s_nop 0
	s_nop 0
	v_add_f32_dpp v1, v1, v1 row_shr:1 row_mask:0xf bank_mask:0xf bound_ctrl:1
	s_nop 1
	v_add_f32_dpp v1, v1, v1 row_shr:2 row_mask:0xf bank_mask:0xf bound_ctrl:1
	s_nop 1
	v_add_f32_dpp v1, v1, v1 row_shr:4 row_mask:0xf bank_mask:0xf bound_ctrl:1
	s_nop 1
	v_add_f32_dpp v1, v1, v1 row_shr:8 row_mask:0xf bank_mask:0xf bound_ctrl:1
	s_nop 1
	v_mov_b32_dpp v25, v1 row_bcast:15 row_mask:0xa bank_mask:0xf
	v_add_f32_e32 v1, v1, v25
	v_mov_b32_e32 v25, 0
	s_nop 1
	v_mov_b32_dpp v25, v1 row_bcast:31 row_mask:0xc bank_mask:0xf
	v_add_f32_e32 v1, v1, v25
	s_nop 0
	s_waitcnt lgkmcnt(11)
	v_pk_mul_f32 v[192:193], v[84:85], v[244:245]
	ds_read_b128 v[240:243], v105 offset:36864
	v_pk_fma_f32 v[192:193], v[72:73], v[246:247], v[192:193]
	v_readlane_b32 s39, v1, 63
	s_nop 0
	s_nop 0
	s_waitcnt lgkmcnt(11)
	v_pk_fma_f32 v[192:193], v[88:89], v[248:249], v[192:193]
	ds_read_b128 v[244:247], v105 offset:37888
	v_pk_fma_f32 v[192:193], v[62:63], v[250:251], v[192:193]
	s_waitcnt lgkmcnt(11)
	v_pk_fma_f32 v[192:193], v[80:81], v[196:197], v[192:193]
	ds_read_b128 v[248:251], v105 offset:38912
	v_pk_fma_f32 v[192:193], v[70:71], v[198:199], v[192:193]
	s_waitcnt lgkmcnt(11)
	v_pk_fma_f32 v[192:193], v[86:87], v[200:201], v[192:193]
	ds_read_b128 v[196:199], v105 offset:39936
	v_pk_fma_f32 v[192:193], v[60:61], v[202:203], v[192:193]
	s_waitcnt lgkmcnt(11)
	v_pk_fma_f32 v[192:193], v[76:77], v[204:205], v[192:193]
	ds_read_b128 v[200:203], v105 offset:40960
	v_pk_fma_f32 v[192:193], v[68:69], v[206:207], v[192:193]
	s_waitcnt lgkmcnt(11)
	v_pk_fma_f32 v[192:193], v[82:83], v[208:209], v[192:193]
	ds_read_b128 v[204:207], v105 offset:41984
	v_pk_fma_f32 v[192:193], v[58:59], v[210:211], v[192:193]
	s_waitcnt lgkmcnt(11)
	v_pk_fma_f32 v[192:193], v[74:75], v[212:213], v[192:193]
	ds_read_b128 v[208:211], v105 offset:43008
	v_pk_fma_f32 v[192:193], v[64:65], v[214:215], v[192:193]
	s_waitcnt lgkmcnt(11)
	v_pk_fma_f32 v[192:193], v[78:79], v[216:217], v[192:193]
	ds_read_b128 v[212:215], v105 offset:44032
	v_pk_fma_f32 v[192:193], v[66:67], v[218:219], v[192:193]
	v_add_f32_e32 v1, v192, v193
	v_mov_b32_e32 v25, 0
	s_nop 0
	s_nop 0
	v_add_f32_dpp v1, v1, v1 row_shr:1 row_mask:0xf bank_mask:0xf bound_ctrl:1
	s_nop 1
	v_add_f32_dpp v1, v1, v1 row_shr:2 row_mask:0xf bank_mask:0xf bound_ctrl:1
	s_nop 1
	v_add_f32_dpp v1, v1, v1 row_shr:4 row_mask:0xf bank_mask:0xf bound_ctrl:1
	s_nop 1
	v_add_f32_dpp v1, v1, v1 row_shr:8 row_mask:0xf bank_mask:0xf bound_ctrl:1
	s_nop 1
	v_mov_b32_dpp v25, v1 row_bcast:15 row_mask:0xa bank_mask:0xf
	v_add_f32_e32 v1, v1, v25
	v_mov_b32_e32 v25, 0
	s_nop 1
	v_mov_b32_dpp v25, v1 row_bcast:31 row_mask:0xc bank_mask:0xf
	v_add_f32_e32 v1, v1, v25
	s_nop 0
	s_waitcnt lgkmcnt(11)
	v_pk_mul_f32 v[190:191], v[84:85], v[220:221]
	ds_read_b128 v[216:219], v105 offset:45056
	v_pk_fma_f32 v[190:191], v[72:73], v[222:223], v[190:191]
	v_readlane_b32 s62, v1, 63
	s_nop 0
	s_nop 0
	s_waitcnt lgkmcnt(11)
	v_pk_fma_f32 v[190:191], v[88:89], v[224:225], v[190:191]
	ds_read_b128 v[220:223], v105 offset:46080
	v_pk_fma_f32 v[190:191], v[62:63], v[226:227], v[190:191]
	s_waitcnt lgkmcnt(11)
	v_pk_fma_f32 v[190:191], v[80:81], v[228:229], v[190:191]
	ds_read_b128 v[224:227], v105 offset:47104
	v_pk_fma_f32 v[190:191], v[70:71], v[230:231], v[190:191]
	s_waitcnt lgkmcnt(11)
	v_pk_fma_f32 v[190:191], v[86:87], v[232:233], v[190:191]
	ds_read_b128 v[228:231], v105 offset:48128
	v_pk_fma_f32 v[190:191], v[60:61], v[234:235], v[190:191]
	s_waitcnt lgkmcnt(11)
	v_pk_fma_f32 v[190:191], v[76:77], v[240:241], v[190:191]
	ds_read_b128 v[232:235], v105 offset:49152
	v_pk_fma_f32 v[190:191], v[68:69], v[242:243], v[190:191]
	s_waitcnt lgkmcnt(11)
	v_pk_fma_f32 v[190:191], v[82:83], v[244:245], v[190:191]
	ds_read_b128 v[240:243], v105 offset:50176
	v_pk_fma_f32 v[190:191], v[58:59], v[246:247], v[190:191]
	s_waitcnt lgkmcnt(11)
	v_pk_fma_f32 v[190:191], v[74:75], v[248:249], v[190:191]
	ds_read_b128 v[244:247], v105 offset:51200
	v_pk_fma_f32 v[190:191], v[64:65], v[250:251], v[190:191]
	s_waitcnt lgkmcnt(11)
	v_pk_fma_f32 v[190:191], v[78:79], v[196:197], v[190:191]
	ds_read_b128 v[248:251], v105 offset:52224
	v_pk_fma_f32 v[190:191], v[66:67], v[198:199], v[190:191]
	v_add_f32_e32 v1, v190, v191
	v_mov_b32_e32 v25, 0
	s_nop 0
	s_nop 0
	v_add_f32_dpp v1, v1, v1 row_shr:1 row_mask:0xf bank_mask:0xf bound_ctrl:1
	s_nop 1
	v_add_f32_dpp v1, v1, v1 row_shr:2 row_mask:0xf bank_mask:0xf bound_ctrl:1
	s_nop 1
	v_add_f32_dpp v1, v1, v1 row_shr:4 row_mask:0xf bank_mask:0xf bound_ctrl:1
	s_nop 1
	v_add_f32_dpp v1, v1, v1 row_shr:8 row_mask:0xf bank_mask:0xf bound_ctrl:1
	s_nop 1
	v_mov_b32_dpp v25, v1 row_bcast:15 row_mask:0xa bank_mask:0xf
	v_add_f32_e32 v1, v1, v25
	v_mov_b32_e32 v25, 0
	s_nop 1
	v_mov_b32_dpp v25, v1 row_bcast:31 row_mask:0xc bank_mask:0xf
	v_add_f32_e32 v1, v1, v25
	s_nop 0
	s_waitcnt lgkmcnt(11)
	v_pk_mul_f32 v[192:193], v[84:85], v[200:201]
	ds_read_b128 v[196:199], v105 offset:53248
	v_pk_fma_f32 v[192:193], v[72:73], v[202:203], v[192:193]
	v_readlane_b32 s63, v1, 63
	s_nop 0
	s_nop 0
	s_waitcnt lgkmcnt(11)
	v_pk_fma_f32 v[192:193], v[88:89], v[204:205], v[192:193]
	ds_read_b128 v[200:203], v105 offset:54272
	v_pk_fma_f32 v[192:193], v[62:63], v[206:207], v[192:193]
	s_waitcnt lgkmcnt(11)
	v_pk_fma_f32 v[192:193], v[80:81], v[208:209], v[192:193]
	ds_read_b128 v[204:207], v105 offset:55296
	v_pk_fma_f32 v[192:193], v[70:71], v[210:211], v[192:193]
	s_waitcnt lgkmcnt(11)
; #define LAS __attribute__((address_space(3)))
; __device__ __forceinline__ float wave_sum(float v) { return lane63(scan64<false>(v)); }
; template <int YMODE, int EXTRA, bool NORM_OUT, bool XN8  , bool XIN_BF = false  , bool XOUT_BF = false  > ...
;     ...
;                     float d8[8];
; #pragma unroll
;                     for (int e = 0; e < 8; ++e) { float s = 0.f;
; #pragma unroll
;                         for (int j = 0; j < 8; ++j) { const f32x4 w = *(const LAS f32x4*)(we + e * D + 256 * j + 4 * F.lane); s += (x[j][0] * w[0] + x[j][1] * w[1]) + (x[j][2] * w[2] + x[j][3] * w[3]); }
;                         d8[e] = wave_sum(s); asm volatile("" ::: "memory"); }
;                     if (EXTRA == 1) {
;                         float v = 0.f;
; #pragma unroll
;                         for (int e = 0; e < 8; ++e) v = (F.lane == e) ? d8[e] : v;
;                         if (F.lane < 8) { const float bb = (F.lane < 4) ? bi[F.lane] : bfg[F.lane - 4]; const float z = 15.f * tanhf((v + bb) * (1.f / 15.f));
;                             const float o = (F.lane < 4) ? z : (fminf(z, 0.f) - log1pf(expf(-fabsf(z)))); gates_out[row * 8 + F.lane] = o; }
	v_pk_fma_f32 v[192:193], v[86:87], v[212:213], v[192:193]
	ds_read_b128 v[208:211], v105 offset:56320
	v_pk_fma_f32 v[192:193], v[60:61], v[214:215], v[192:193]
	s_waitcnt lgkmcnt(11)
	v_pk_fma_f32 v[192:193], v[76:77], v[216:217], v[192:193]
	ds_read_b128 v[212:215], v105 offset:57344
	v_pk_fma_f32 v[192:193], v[68:69], v[218:219], v[192:193]
	s_waitcnt lgkmcnt(11)
	v_pk_fma_f32 v[192:193], v[82:83], v[220:221], v[192:193]
	ds_read_b128 v[216:219], v105 offset:58368
	v_pk_fma_f32 v[192:193], v[58:59], v[222:223], v[192:193]
	s_waitcnt lgkmcnt(11)
	v_pk_fma_f32 v[192:193], v[74:75], v[224:225], v[192:193]
	ds_read_b128 v[220:223], v105 offset:59392
	v_pk_fma_f32 v[192:193], v[64:65], v[226:227], v[192:193]
	s_waitcnt lgkmcnt(11)
	v_pk_fma_f32 v[192:193], v[78:79], v[228:229], v[192:193]
	ds_read_b128 v[224:227], v105 offset:60416
	v_pk_fma_f32 v[192:193], v[66:67], v[230:231], v[192:193]
	v_add_f32_e32 v1, v192, v193
	v_mov_b32_e32 v25, 0
	s_nop 0
	s_nop 0
	v_add_f32_dpp v1, v1, v1 row_shr:1 row_mask:0xf bank_mask:0xf bound_ctrl:1
	s_nop 1
	v_add_f32_dpp v1, v1, v1 row_shr:2 row_mask:0xf bank_mask:0xf bound_ctrl:1
	s_nop 1
	v_add_f32_dpp v1, v1, v1 row_shr:4 row_mask:0xf bank_mask:0xf bound_ctrl:1
	s_nop 1
	v_add_f32_dpp v1, v1, v1 row_shr:8 row_mask:0xf bank_mask:0xf bound_ctrl:1
	s_nop 1
	v_mov_b32_dpp v25, v1 row_bcast:15 row_mask:0xa bank_mask:0xf
	v_add_f32_e32 v1, v1, v25
	v_mov_b32_e32 v25, 0
	s_nop 1
	v_mov_b32_dpp v25, v1 row_bcast:31 row_mask:0xc bank_mask:0xf
	v_add_f32_e32 v1, v1, v25
	s_nop 0
	s_waitcnt lgkmcnt(11)
	v_pk_mul_f32 v[190:191], v[84:85], v[232:233]
	ds_read_b128 v[228:231], v105 offset:61440
	v_pk_fma_f32 v[190:191], v[72:73], v[234:235], v[190:191]
	v_readlane_b32 s66, v1, 63
	s_nop 0
	s_nop 0
	s_waitcnt lgkmcnt(11)
	v_pk_fma_f32 v[190:191], v[88:89], v[240:241], v[190:191]
	ds_read_b128 v[232:235], v105 offset:62464
	v_pk_fma_f32 v[190:191], v[62:63], v[242:243], v[190:191]
	s_waitcnt lgkmcnt(11)
	v_pk_fma_f32 v[190:191], v[80:81], v[244:245], v[190:191]
	ds_read_b128 v[240:243], v105 offset:63488
	v_pk_fma_f32 v[190:191], v[70:71], v[246:247], v[190:191]
	s_waitcnt lgkmcnt(11)
	v_pk_fma_f32 v[190:191], v[86:87], v[248:249], v[190:191]
	ds_read_b128 v[244:247], v105 offset:64512
	v_pk_fma_f32 v[190:191], v[60:61], v[250:251], v[190:191]
	s_waitcnt lgkmcnt(11)
	v_pk_fma_f32 v[190:191], v[76:77], v[196:197], v[190:191]
	v_pk_fma_f32 v[190:191], v[68:69], v[198:199], v[190:191]
	s_waitcnt lgkmcnt(10)
	v_pk_fma_f32 v[190:191], v[82:83], v[200:201], v[190:191]
	v_pk_fma_f32 v[190:191], v[58:59], v[202:203], v[190:191]
	s_waitcnt lgkmcnt(9)
	v_pk_fma_f32 v[190:191], v[74:75], v[204:205], v[190:191]
	v_pk_fma_f32 v[190:191], v[64:65], v[206:207], v[190:191]
	s_nop 0
	s_waitcnt lgkmcnt(8)
	v_pk_fma_f32 v[190:191], v[78:79], v[208:209], v[190:191]
	v_pk_fma_f32 v[190:191], v[66:67], v[210:211], v[190:191]
	v_add_f32_e32 v1, v190, v191
	v_mov_b32_e32 v25, 0
	s_nop 0
	s_nop 0
	v_add_f32_dpp v1, v1, v1 row_shr:1 row_mask:0xf bank_mask:0xf bound_ctrl:1
	s_nop 0
	s_waitcnt lgkmcnt(6)
	v_pk_mul_f32 v[192:193], v[88:89], v[216:217]
	v_pk_fma_f32 v[192:193], v[62:63], v[218:219], v[192:193]
	v_add_f32_dpp v1, v1, v1 row_shr:2 row_mask:0xf bank_mask:0xf bound_ctrl:1
	s_nop 0
	s_nop 0
	v_add_f32_dpp v1, v1, v1 row_shr:4 row_mask:0xf bank_mask:0xf bound_ctrl:1
	s_nop 1
	v_add_f32_dpp v1, v1, v1 row_shr:8 row_mask:0xf bank_mask:0xf bound_ctrl:1
	s_nop 1
	v_mov_b32_dpp v25, v1 row_bcast:15 row_mask:0xa bank_mask:0xf
	v_add_f32_e32 v1, v1, v25
	v_mov_b32_e32 v25, 0
	s_nop 1
	v_mov_b32_dpp v25, v1 row_bcast:31 row_mask:0xc bank_mask:0xf
	v_add_f32_e32 v1, v1, v25
	v_pk_fma_f32 v[192:193], v[84:85], v[212:213], v[192:193]
	v_pk_fma_f32 v[192:193], v[72:73], v[214:215], v[192:193]
	v_readlane_b32 s67, v1, 63
	s_nop 0
	s_nop 0
	s_nop 0
	s_waitcnt lgkmcnt(5)
	v_pk_fma_f32 v[192:193], v[80:81], v[220:221], v[192:193]
	v_pk_fma_f32 v[192:193], v[70:71], v[222:223], v[192:193]
	s_waitcnt lgkmcnt(4)
	v_pk_fma_f32 v[192:193], v[86:87], v[224:225], v[192:193]
	v_pk_fma_f32 v[192:193], v[60:61], v[226:227], v[192:193]
	s_waitcnt lgkmcnt(3)
	v_pk_fma_f32 v[192:193], v[76:77], v[228:229], v[192:193]
	v_pk_fma_f32 v[192:193], v[68:69], v[230:231], v[192:193]
	s_waitcnt lgkmcnt(2)
	v_pk_fma_f32 v[192:193], v[82:83], v[232:233], v[192:193]
	v_pk_fma_f32 v[192:193], v[58:59], v[234:235], v[192:193]
	s_waitcnt lgkmcnt(1)
	v_pk_fma_f32 v[192:193], v[74:75], v[240:241], v[192:193]
	v_pk_fma_f32 v[192:193], v[64:65], v[242:243], v[192:193]
	s_waitcnt lgkmcnt(0)
	v_pk_fma_f32 v[192:193], v[78:79], v[244:245], v[192:193]
	v_pk_fma_f32 v[192:193], v[66:67], v[246:247], v[192:193]
	v_add_f32_e32 v1, v192, v193
	v_mov_b32_e32 v25, 0
	s_nop 0
	v_add_f32_dpp v1, v1, v1 row_shr:1 row_mask:0xf bank_mask:0xf bound_ctrl:1
	s_nop 1
	v_add_f32_dpp v1, v1, v1 row_shr:2 row_mask:0xf bank_mask:0xf bound_ctrl:1
	s_nop 1
	v_add_f32_dpp v1, v1, v1 row_shr:4 row_mask:0xf bank_mask:0xf bound_ctrl:1
	s_nop 1
	v_add_f32_dpp v1, v1, v1 row_shr:8 row_mask:0xf bank_mask:0xf bound_ctrl:1
	s_nop 1
	v_mov_b32_dpp v25, v1 row_bcast:15 row_mask:0xa bank_mask:0xf
	v_add_f32_e32 v1, v1, v25
	v_mov_b32_e32 v25, 0
	s_nop 1
	v_mov_b32_dpp v25, v1 row_bcast:31 row_mask:0xc bank_mask:0xf
	v_add_f32_e32 v1, v1, v25
	s_nop 0
	v_readlane_b32 s68, v1, 63
	s_and_saveexec_b64 s[26:27], s[8:9]
	s_cbranch_execz .LBB0_1306
	v_mov_b32_e32 v1, s34
	v_cndmask_b32_e64 v1, 0, v1, s[6:7]
	v_mov_b32_e32 v25, s38
	v_cndmask_b32_e64 v1, v1, v25, s[22:23]
	v_mov_b32_e32 v25, s39
	v_cndmask_b32_e64 v1, v1, v25, s[20:21]
	v_mov_b32_e32 v25, s62
	v_cndmask_b32_e64 v1, v1, v25, s[18:19]
	v_mov_b32_e32 v25, s63
	v_cndmask_b32_e64 v1, v1, v25, s[16:17]
	v_mov_b32_e32 v25, s66
	v_cndmask_b32_e64 v1, v1, v25, s[14:15]
	v_mov_b32_e32 v25, s67
	v_cndmask_b32_e64 v1, v1, v25, s[12:13]
	v_mov_b32_e32 v25, s68
	v_cndmask_b32_e64 v1, v1, v25, s[10:11]
	s_mov_b32 s34, 0x3f200000
	s_waitcnt lgkmcnt(0)
	v_add_f32_e32 v1, v1, v179
	v_mul_f32_e32 v1, 0x3d888889, v1
	v_cmp_nlt_f32_e64 s[38:39], |v1|, s34
	s_and_saveexec_b64 s[62:63], s[38:39]
	s_xor_b64 s[38:39], exec, s[62:63]
	s_cbranch_execz .LBB0_1314
	v_add_f32_e64 v25, |v1|, |v1|
	v_mul_f32_e32 v58, 0x3fb8aa3b, v25
	v_rndne_f32_e32 v59, v58
	s_mov_b32 s34, 0x3fb8aa3b
	v_sub_f32_e32 v60, v58, v59
	v_fma_f32 v58, v25, s34, -v58
	v_fmac_f32_e32 v58, 0x32a5705f, v25
	v_add_f32_e32 v58, v60, v58
	v_cvt_i32_f32_e32 v59, v59
	v_exp_f32_e32 v58, v58
	s_mov_b32 s34, 0xc2ce8ed0
	v_cmp_ngt_f32_e32 vcc, s34, v25
	v_ldexp_f32 v58, v58, v59
	s_nop 0
	v_cndmask_b32_e32 v58, 0, v58, vcc
	v_cmp_nlt_f32_e32 vcc, s44, v25
	s_nop 1
	v_cndmask_b32_e32 v25, v111, v58, vcc
	v_add_f32_e32 v25, 1.0, v25
	v_rcp_f32_e32 v25, v25
	s_nop 0
	v_fma_f32 v25, v25, -2.0, 1.0
